# v13 + SwiGLU epilogue split in all three fp8 up-projection GEMMs: second half deferred into the next unit's first K-tile (3/8 under its MFMAs)
# baseline (speedup 1.0000x reference)
.LBB0_809:
	v_bfe_u32 v165, v168, 4, 2
	v_and_b32_e32 v1, 15, v168
	v_lshlrev_b32_e32 v6, 4, v165
	v_lshlrev_b32_e32 v7, 2, v168
	s_lshl_b32 s73, s4, 6
	v_lshl_or_b32 v6, v1, 6, v6
	s_lshl_b32 s4, s4, 13
	v_and_b32_e32 v7, 32, v7
	v_bitop3_b32 v8, v6, s4, v7 bitop3:0xde
	s_lshl_b32 s4, s5, 5
	v_mov_b32_e32 v171, v35
	s_and_b32 s74, s4, 0x60
	v_lshl_add_u64 v[2:3], s[30:31], 0, v[170:171]
	v_mov_b32_e32 v173, v35
	s_lshl_b32 s4, s74, 7
	v_lshl_add_u64 v[4:5], s[30:31], 0, v[172:173]
	v_bitop3_b32 v167, v6, s4, v7 bitop3:0xde
	s_add_i32 m0, s69, 0x18000
	v_lshl_add_u64 v[2:3], v[2:3], 0, s[18:19]
	v_readlane_b32 s4, v253, 28
	s_waitcnt vmcnt(2)
	s_barrier
	global_load_lds_dwordx4 v[2:3], off
	v_lshl_add_u64 v[2:3], v[4:5], 0, s[18:19]
	s_add_i32 m0, s69, 0x1a000
	v_readlane_b32 s5, v253, 29
	s_add_i32 s75, s69, 0x8000
	v_mov_b32_e32 v193, v35
	global_load_lds_dwordx4 v[2:3], off
	v_lshl_add_u64 v[2:3], s[4:5], 0, v[34:35]
	s_mov_b32 m0, s75
	s_add_i32 s76, s69, 0xa000
	global_load_lds_dwordx4 v[2:3], off
	v_lshl_add_u64 v[2:3], s[4:5], 0, v[192:193]
	s_add_u32 s4, s30, 0x20080
	s_mov_b32 m0, s76
	s_addc_u32 s5, s31, 0
	global_load_lds_dwordx4 v[2:3], off
	s_add_i32 m0, s69, 0x1c000
	v_lshl_add_u64 v[2:3], s[4:5], 0, v[170:171]
	global_load_lds_dwordx4 v[2:3], off
	v_lshl_add_u64 v[2:3], s[4:5], 0, v[172:173]
	s_add_i32 m0, s69, 0x1e000
	v_mov_b32_e32 v36, 0
	global_load_lds_dwordx4 v[2:3], off
	s_waitcnt vmcnt(6)
	s_cmpk_lt_u32 s16, 0x100
	s_mov_b32 s77, 0
	s_cselect_b64 s[16:17], -1, 0
	v_add_u32_e32 v169, 0, v8
	v_mov_b32_e32 v198, v174
	v_mov_b32_e32 v189, v190
	v_mov_b32_e32 v37, v36
	v_mov_b32_e32 v38, v36
	v_mov_b32_e32 v39, v36
	v_mov_b32_e32 v40, v36
	v_mov_b32_e32 v41, v36
	v_mov_b32_e32 v42, v36
	v_mov_b32_e32 v43, v36
	v_mov_b32_e32 v44, v36
	v_mov_b32_e32 v45, v36
	v_mov_b32_e32 v46, v36
	v_mov_b32_e32 v47, v36
	v_mov_b32_e32 v48, v36
	v_mov_b32_e32 v49, v36
	v_mov_b32_e32 v50, v36
	v_mov_b32_e32 v51, v36
	v_mov_b32_e32 v52, v36
	v_mov_b32_e32 v53, v36
	v_mov_b32_e32 v54, v36
	v_mov_b32_e32 v55, v36
	v_mov_b32_e32 v56, v36
	v_mov_b32_e32 v57, v36
	v_mov_b32_e32 v58, v36
	v_mov_b32_e32 v59, v36
	v_mov_b32_e32 v60, v36
	v_mov_b32_e32 v61, v36
	v_mov_b32_e32 v62, v36
	v_mov_b32_e32 v63, v36
	v_mov_b32_e32 v64, v36
	v_mov_b32_e32 v65, v36
	v_mov_b32_e32 v66, v36
	v_mov_b32_e32 v67, v36
	v_mov_b32_e32 v68, v36
	v_mov_b32_e32 v69, v36
	v_mov_b32_e32 v70, v36
	v_mov_b32_e32 v71, v36
	v_mov_b32_e32 v72, v36
	v_mov_b32_e32 v73, v36
	v_mov_b32_e32 v74, v36
	v_mov_b32_e32 v75, v36
	v_mov_b32_e32 v76, v36
	v_mov_b32_e32 v77, v36
	v_mov_b32_e32 v78, v36
	v_mov_b32_e32 v79, v36
	v_mov_b32_e32 v80, v36
	v_mov_b32_e32 v81, v36
	v_mov_b32_e32 v82, v36
	v_mov_b32_e32 v83, v36
	v_mov_b32_e32 v84, v36
	v_mov_b32_e32 v85, v36
	v_mov_b32_e32 v86, v36
	v_mov_b32_e32 v87, v36
	v_mov_b32_e32 v88, v36
	v_mov_b32_e32 v89, v36
	v_mov_b32_e32 v90, v36
	v_mov_b32_e32 v91, v36
	v_mov_b32_e32 v92, v36
	v_mov_b32_e32 v93, v36
	v_mov_b32_e32 v94, v36
	v_mov_b32_e32 v95, v36
	v_mov_b32_e32 v96, v36
	v_mov_b32_e32 v97, v36
	v_mov_b32_e32 v98, v36
	v_mov_b32_e32 v99, v36
	v_mov_b32_e32 v100, v36
	v_mov_b32_e32 v101, v36
	v_mov_b32_e32 v102, v36
	v_mov_b32_e32 v103, v36
	v_mov_b32_e32 v104, v36
	v_mov_b32_e32 v105, v36
	v_mov_b32_e32 v106, v36
	v_mov_b32_e32 v107, v36
	v_mov_b32_e32 v108, v36
	v_mov_b32_e32 v109, v36
	v_mov_b32_e32 v110, v36
	v_mov_b32_e32 v111, v36
	v_mov_b32_e32 v112, v36
	v_mov_b32_e32 v113, v36
	v_mov_b32_e32 v114, v36
	v_mov_b32_e32 v115, v36
	v_mov_b32_e32 v116, v36
	v_mov_b32_e32 v117, v36
	v_mov_b32_e32 v118, v36
	v_mov_b32_e32 v119, v36
	v_mov_b32_e32 v120, v36
	v_mov_b32_e32 v121, v36
	v_mov_b32_e32 v122, v36
	v_mov_b32_e32 v123, v36
	v_mov_b32_e32 v124, v36
	v_mov_b32_e32 v125, v36
	v_mov_b32_e32 v126, v36
	v_mov_b32_e32 v127, v36
	v_mov_b32_e32 v128, v36
	v_mov_b32_e32 v129, v36
	v_mov_b32_e32 v130, v36
	v_mov_b32_e32 v131, v36
	v_mov_b32_e32 v132, v36
	v_mov_b32_e32 v133, v36
	v_mov_b32_e32 v134, v36
	v_mov_b32_e32 v135, v36
	v_mov_b32_e32 v136, v36
	v_mov_b32_e32 v137, v36
	v_mov_b32_e32 v138, v36
	v_mov_b32_e32 v139, v36
	v_mov_b32_e32 v140, v36
	v_mov_b32_e32 v141, v36
	v_mov_b32_e32 v142, v36
	v_mov_b32_e32 v143, v36
	v_mov_b32_e32 v144, v36
	v_mov_b32_e32 v145, v36
	v_mov_b32_e32 v146, v36
	v_mov_b32_e32 v147, v36
	v_mov_b32_e32 v148, v36
	v_mov_b32_e32 v149, v36
	v_mov_b32_e32 v150, v36
	v_mov_b32_e32 v151, v36
	v_mov_b32_e32 v152, v36
	v_mov_b32_e32 v153, v36
	v_mov_b32_e32 v154, v36
	v_mov_b32_e32 v155, v36
	v_mov_b32_e32 v156, v36
	v_mov_b32_e32 v157, v36
	v_mov_b32_e32 v158, v36
	v_mov_b32_e32 v159, v36
	v_mov_b32_e32 v160, v36
	v_mov_b32_e32 v161, v36
	v_mov_b32_e32 v162, v36
	v_mov_b32_e32 v163, v36
	s_barrier
	s_mov_b32 s32, 0
	s_branch .LBB0_811

.LBB0_819:
	s_add_u32 s81, s30, 0x200
	s_addc_u32 s82, s31, 0
	s_add_i32 s55, 0, 0x14000
	s_add_i32 s52, 0, 0x10000
	v_add_u32_e32 v199, s55, v167
	v_add_u32_e32 v200, s52, v167
	ds_read_b128 v[10:13], v199
	ds_read_b128 v[14:17], v199 offset:1024
	ds_read_b128 v[2:5], v199 offset:2048
	ds_read_b128 v[6:9], v199 offset:3072
	ds_read_b128 v[22:25], v200 offset:3072
	ds_read_b128 v[18:21], v200 offset:2048
	ds_read_b128 v[30:33], v200 offset:1024
	ds_read_b128 v[26:29], v200
	s_lshl_b32 s14, s80, 10
	s_add_i32 s83, s14, 0
	s_add_i32 s83, s83, 0x20400
	v_mov_b32_e32 v191, v35
	v_mov_b32_e32 v175, v35
	s_add_i32 s84, s69, 0xc000
	v_readlane_b32 s26, v253, 28
	s_mov_b32 m0, s84
	v_readlane_b32 s27, v253, 29
	s_add_i32 s53, s69, 0xe000
	ds_read_b128 v[202:205], v169
	ds_read_b128 v[206:209], v169 offset:1024
	ds_read_b128 v[222:225], v169 offset:2048
	ds_read_b128 v[226:229], v169 offset:3072
	ds_read_b128 v[230:233], v169 offset:4096
	ds_read_b128 v[234:237], v169 offset:5120
	ds_read_b128 v[238:241], v169 offset:6144
	ds_read_b128 v[242:245], v169 offset:7168
	global_load_lds_dwordx4 v190, s[26:27]
	s_mov_b32 m0, s53
	s_nop 0
	global_load_lds_dwordx4 v174, s[26:27]
	s_waitcnt vmcnt(8)
	s_waitcnt lgkmcnt(0)
	s_barrier
	s_setprio 1
	s_waitcnt lgkmcnt(0)
	s_mov_b32 vcc_lo, s32
	s_mov_b32 vcc_hi, 0
	s_cbranch_vccz .Lc1p_m0
	v_mfma_f32_16x16x128_f8f6f4 v[160:163], v[26:33], v[202:209], 0
	v_exp_f32_e64 v212, -v96
	v_exp_f32_e64 v213, -v97
	v_exp_f32_e64 v214, -v98
	v_exp_f32_e64 v215, -v99
	v_pk_mul_f32 v[216:217], v[96:97], v[64:65]
	v_mfma_f32_16x16x128_f8f6f4 v[156:159], v[18:25], v[202:209], 0
	v_pk_mul_f32 v[218:219], v[98:99], v[66:67]
	v_pk_add_f32 v[212:213], v[212:213], 1.0 op_sel_hi:[1,0]
	v_pk_add_f32 v[214:215], v[214:215], 1.0 op_sel_hi:[1,0]
	v_rcp_f32_e32 v212, v212
	v_rcp_f32_e32 v213, v213
	v_mfma_f32_16x16x128_f8f6f4 v[148:151], v[18:25], v[222:229], 0
	v_rcp_f32_e32 v214, v214
	v_rcp_f32_e32 v215, v215
	v_mov_b32_e32 v180, v35
	v_pk_mul_f32 v[216:217], v[212:213], v[216:217]
	v_pk_mul_f32 v[218:219], v[214:215], v[218:219]
	v_mfma_f32_16x16x128_f8f6f4 v[152:155], v[26:33], v[222:229], 0
	v_med3_f32 v216, v216, s13, v250
	v_med3_f32 v217, v217, s13, v250
	v_med3_f32 v218, v218, s13, v250
	v_med3_f32 v219, v219, s13, v250
	v_cvt_pk_fp8_f32 v180, v216, v217
	v_mfma_f32_16x16x128_f8f6f4 v[144:147], v[26:33], v[230:237], 0
	s_nop 0
	v_cvt_pk_fp8_f32 v180, v218, v219 op_sel:[0,0,1]
	v_exp_f32_e64 v212, -v92
	v_exp_f32_e64 v213, -v93
	v_exp_f32_e64 v214, -v94
	v_mfma_f32_16x16x128_f8f6f4 v[140:143], v[18:25], v[230:237], 0
	v_exp_f32_e64 v215, -v95
	v_pk_mul_f32 v[216:217], v[92:93], v[60:61]
	v_pk_mul_f32 v[218:219], v[94:95], v[62:63]
	v_pk_add_f32 v[212:213], v[212:213], 1.0 op_sel_hi:[1,0]
	v_pk_add_f32 v[214:215], v[214:215], 1.0 op_sel_hi:[1,0]
	v_mfma_f32_16x16x128_f8f6f4 v[132:135], v[18:25], v[238:245], 0
	v_rcp_f32_e32 v212, v212
	v_rcp_f32_e32 v213, v213
	v_rcp_f32_e32 v214, v214
	v_rcp_f32_e32 v215, v215
	v_mov_b32_e32 v181, v35
	v_mfma_f32_16x16x128_f8f6f4 v[136:139], v[26:33], v[238:245], 0
	v_pk_mul_f32 v[216:217], v[212:213], v[216:217]
	v_pk_mul_f32 v[218:219], v[214:215], v[218:219]
	v_med3_f32 v216, v216, s13, v250
	v_med3_f32 v217, v217, s13, v250
	v_med3_f32 v218, v218, s13, v250
	s_setprio 0
	s_setprio 1
	v_mfma_f32_16x16x128_f8f6f4 v[128:131], v[10:17], v[202:209], 0
	v_med3_f32 v219, v219, s13, v250
	v_cvt_pk_fp8_f32 v181, v216, v217
	s_nop 0
	v_cvt_pk_fp8_f32 v181, v218, v219 op_sel:[0,0,1]
	s_nop 0
	v_mfma_f32_16x16x128_f8f6f4 v[124:127], v[2:9], v[202:209], 0
	global_store_dwordx2 v[182:183], v[180:181], off
	v_add_co_u32_e32 v182, vcc, 0xe000, v182
	s_nop 1
	v_addc_co_u32_e32 v183, vcc, 0, v183, vcc
	v_exp_f32_e64 v212, -v88
	v_mfma_f32_16x16x128_f8f6f4 v[116:119], v[2:9], v[222:229], 0
	v_exp_f32_e64 v213, -v89
	v_exp_f32_e64 v214, -v90
	v_exp_f32_e64 v215, -v91
	v_pk_mul_f32 v[216:217], v[88:89], v[56:57]
	v_pk_mul_f32 v[218:219], v[90:91], v[58:59]
	v_mfma_f32_16x16x128_f8f6f4 v[120:123], v[10:17], v[222:229], 0
	v_pk_add_f32 v[212:213], v[212:213], 1.0 op_sel_hi:[1,0]
	v_pk_add_f32 v[214:215], v[214:215], 1.0 op_sel_hi:[1,0]
	v_rcp_f32_e32 v212, v212
	v_rcp_f32_e32 v213, v213
	v_rcp_f32_e32 v214, v214
	v_mfma_f32_16x16x128_f8f6f4 v[112:115], v[10:17], v[230:237], 0
	v_rcp_f32_e32 v215, v215
	v_mov_b32_e32 v180, v35
	v_pk_mul_f32 v[216:217], v[212:213], v[216:217]
	v_pk_mul_f32 v[218:219], v[214:215], v[218:219]
	v_med3_f32 v216, v216, s13, v250
	v_mfma_f32_16x16x128_f8f6f4 v[108:111], v[2:9], v[230:237], 0
	v_med3_f32 v217, v217, s13, v250
	v_med3_f32 v218, v218, s13, v250
	v_med3_f32 v219, v219, s13, v250
	v_cvt_pk_fp8_f32 v180, v216, v217
	s_nop 0
	v_mfma_f32_16x16x128_f8f6f4 v[100:103], v[2:9], v[238:245], 0
	v_cvt_pk_fp8_f32 v180, v218, v219 op_sel:[0,0,1]
	v_mfma_f32_16x16x128_f8f6f4 v[104:107], v[10:17], v[238:245], 0
	s_branch .Lc1d_m0
.Lc1p_m0:
	v_mfma_f32_16x16x128_f8f6f4 v[160:163], v[26:33], v[202:209], 0
	v_mfma_f32_16x16x128_f8f6f4 v[156:159], v[18:25], v[202:209], 0
	v_mfma_f32_16x16x128_f8f6f4 v[148:151], v[18:25], v[222:229], 0
	v_mfma_f32_16x16x128_f8f6f4 v[152:155], v[26:33], v[222:229], 0
	v_mfma_f32_16x16x128_f8f6f4 v[144:147], v[26:33], v[230:237], 0
	v_mfma_f32_16x16x128_f8f6f4 v[140:143], v[18:25], v[230:237], 0
	v_mfma_f32_16x16x128_f8f6f4 v[132:135], v[18:25], v[238:245], 0
	v_mfma_f32_16x16x128_f8f6f4 v[136:139], v[26:33], v[238:245], 0
	s_setprio 0
	s_setprio 1
	v_mfma_f32_16x16x128_f8f6f4 v[128:131], v[10:17], v[202:209], 0
	v_mfma_f32_16x16x128_f8f6f4 v[124:127], v[2:9], v[202:209], 0
	v_mfma_f32_16x16x128_f8f6f4 v[116:119], v[2:9], v[222:229], 0
	v_mfma_f32_16x16x128_f8f6f4 v[120:123], v[10:17], v[222:229], 0
	v_mfma_f32_16x16x128_f8f6f4 v[112:115], v[10:17], v[230:237], 0
	v_mfma_f32_16x16x128_f8f6f4 v[108:111], v[2:9], v[230:237], 0
	v_mfma_f32_16x16x128_f8f6f4 v[100:103], v[2:9], v[238:245], 0
	v_mfma_f32_16x16x128_f8f6f4 v[104:107], v[10:17], v[238:245], 0
.Lc1d_m0:
	s_setprio 0
	s_barrier
	s_add_i32 s52, s52, s68
	v_lshl_add_u64 v[194:195], s[30:31], 0, v[170:171]
	s_add_i32 s85, s52, 0x2000
	v_lshl_add_u64 v[178:179], v[194:195], 0, s[28:29]
	s_mov_b32 m0, s52
	v_lshl_add_u64 v[196:197], s[30:31], 0, v[172:173]
	s_add_u32 s36, s30, 0x20100
	ds_read_b128 v[202:205], v169 offset:16384
	ds_read_b128 v[206:209], v169 offset:17408
	ds_read_b128 v[222:225], v169 offset:18432
	ds_read_b128 v[226:229], v169 offset:19456
	ds_read_b128 v[230:233], v169 offset:20480
	ds_read_b128 v[234:237], v169 offset:21504
	ds_read_b128 v[238:241], v169 offset:22528
	ds_read_b128 v[242:245], v169 offset:23552
	s_mov_b32 vcc_lo, s32
	s_mov_b32 vcc_hi, 0
	s_cbranch_vccz .Le1skip_m0
	v_exp_f32_e64 v212, -v84
	v_exp_f32_e64 v213, -v85
	v_exp_f32_e64 v214, -v86
	v_exp_f32_e64 v215, -v87
	v_pk_mul_f32 v[216:217], v[84:85], v[52:53]
	v_pk_mul_f32 v[218:219], v[86:87], v[54:55]
	v_pk_add_f32 v[212:213], v[212:213], 1.0 op_sel_hi:[1,0]
	v_pk_add_f32 v[214:215], v[214:215], 1.0 op_sel_hi:[1,0]
	v_rcp_f32_e32 v212, v212
	v_rcp_f32_e32 v213, v213
	v_rcp_f32_e32 v214, v214
	v_rcp_f32_e32 v215, v215
	v_mov_b32_e32 v181, v35
	v_pk_mul_f32 v[216:217], v[212:213], v[216:217]
	v_pk_mul_f32 v[218:219], v[214:215], v[218:219]
	v_med3_f32 v216, v216, s13, v250
	v_med3_f32 v217, v217, s13, v250
	v_med3_f32 v218, v218, s13, v250
	v_med3_f32 v219, v219, s13, v250
	v_cvt_pk_fp8_f32 v181, v216, v217
	s_nop 0
	v_cvt_pk_fp8_f32 v181, v218, v219 op_sel:[0,0,1]
	s_nop 0
	global_store_dwordx2 v[182:183], v[180:181], off
	v_add_co_u32_e32 v182, vcc, 0xe000, v182
	s_nop 1
	v_addc_co_u32_e32 v183, vcc, 0, v183, vcc
	v_exp_f32_e64 v212, -v80
	v_exp_f32_e64 v213, -v81
	v_exp_f32_e64 v214, -v82
	v_exp_f32_e64 v215, -v83
	v_pk_mul_f32 v[216:217], v[80:81], v[48:49]
	v_pk_mul_f32 v[218:219], v[82:83], v[50:51]
	v_pk_add_f32 v[212:213], v[212:213], 1.0 op_sel_hi:[1,0]
	v_pk_add_f32 v[214:215], v[214:215], 1.0 op_sel_hi:[1,0]
	v_rcp_f32_e32 v212, v212
	v_rcp_f32_e32 v213, v213
	v_rcp_f32_e32 v214, v214
	v_rcp_f32_e32 v215, v215
	v_mov_b32_e32 v180, v35
	v_pk_mul_f32 v[216:217], v[212:213], v[216:217]
	v_pk_mul_f32 v[218:219], v[214:215], v[218:219]
	v_med3_f32 v216, v216, s13, v250
	v_med3_f32 v217, v217, s13, v250
	v_med3_f32 v218, v218, s13, v250
	v_med3_f32 v219, v219, s13, v250
	v_cvt_pk_fp8_f32 v180, v216, v217
	s_nop 0
	v_cvt_pk_fp8_f32 v180, v218, v219 op_sel:[0,0,1]
	v_exp_f32_e64 v212, -v76
	v_exp_f32_e64 v213, -v77
	v_exp_f32_e64 v214, -v78
	v_exp_f32_e64 v215, -v79
	v_pk_mul_f32 v[216:217], v[76:77], v[44:45]
	v_pk_mul_f32 v[218:219], v[78:79], v[46:47]
	v_pk_add_f32 v[212:213], v[212:213], 1.0 op_sel_hi:[1,0]
	v_pk_add_f32 v[214:215], v[214:215], 1.0 op_sel_hi:[1,0]
	v_rcp_f32_e32 v212, v212
	v_rcp_f32_e32 v213, v213
	v_rcp_f32_e32 v214, v214
	v_rcp_f32_e32 v215, v215
	v_mov_b32_e32 v181, v35
	v_pk_mul_f32 v[216:217], v[212:213], v[216:217]
	v_pk_mul_f32 v[218:219], v[214:215], v[218:219]
	v_med3_f32 v216, v216, s13, v250
	v_med3_f32 v217, v217, s13, v250
	v_med3_f32 v218, v218, s13, v250
	v_med3_f32 v219, v219, s13, v250
	v_cvt_pk_fp8_f32 v181, v216, v217
	s_nop 0
	v_cvt_pk_fp8_f32 v181, v218, v219 op_sel:[0,0,1]
	s_nop 0
	global_store_dwordx2 v[182:183], v[180:181], off
	v_add_co_u32_e32 v182, vcc, 0xe000, v182
	s_nop 1
	v_addc_co_u32_e32 v183, vcc, 0, v183, vcc
	v_exp_f32_e64 v212, -v72
	v_exp_f32_e64 v213, -v73
	v_exp_f32_e64 v214, -v74
	v_exp_f32_e64 v215, -v75
	v_pk_mul_f32 v[216:217], v[72:73], v[40:41]
	v_pk_mul_f32 v[218:219], v[74:75], v[42:43]
	v_pk_add_f32 v[212:213], v[212:213], 1.0 op_sel_hi:[1,0]
	v_pk_add_f32 v[214:215], v[214:215], 1.0 op_sel_hi:[1,0]
	v_rcp_f32_e32 v212, v212
	v_rcp_f32_e32 v213, v213
	v_rcp_f32_e32 v214, v214
	v_rcp_f32_e32 v215, v215
	v_mov_b32_e32 v180, v35
	v_pk_mul_f32 v[216:217], v[212:213], v[216:217]
	v_pk_mul_f32 v[218:219], v[214:215], v[218:219]
	v_med3_f32 v216, v216, s13, v250
	v_med3_f32 v217, v217, s13, v250
	v_med3_f32 v218, v218, s13, v250
	v_med3_f32 v219, v219, s13, v250
	v_cvt_pk_fp8_f32 v180, v216, v217
	s_nop 0
	v_cvt_pk_fp8_f32 v180, v218, v219 op_sel:[0,0,1]
	v_exp_f32_e64 v212, -v68
	v_exp_f32_e64 v213, -v69
	v_exp_f32_e64 v214, -v70
	v_exp_f32_e64 v215, -v71
	v_pk_mul_f32 v[216:217], v[68:69], v[36:37]
	v_pk_mul_f32 v[218:219], v[70:71], v[38:39]
	v_pk_add_f32 v[212:213], v[212:213], 1.0 op_sel_hi:[1,0]
	v_pk_add_f32 v[214:215], v[214:215], 1.0 op_sel_hi:[1,0]
	v_rcp_f32_e32 v212, v212
	v_rcp_f32_e32 v213, v213
	v_rcp_f32_e32 v214, v214
	v_rcp_f32_e32 v215, v215
	v_mov_b32_e32 v181, v35
	v_pk_mul_f32 v[216:217], v[212:213], v[216:217]
	v_pk_mul_f32 v[218:219], v[214:215], v[218:219]
	v_med3_f32 v216, v216, s13, v250
	v_med3_f32 v217, v217, s13, v250
	v_med3_f32 v218, v218, s13, v250
	v_med3_f32 v219, v219, s13, v250
	v_cvt_pk_fp8_f32 v181, v216, v217
	s_nop 0
	v_cvt_pk_fp8_f32 v181, v218, v219 op_sel:[0,0,1]
	s_nop 0
	global_store_dwordx2 v[182:183], v[180:181], off
.Le1skip_m0:
	global_load_lds_dwordx4 v[178:179], off
	v_lshl_add_u64 v[178:179], v[196:197], 0, s[28:29]
	s_mov_b32 m0, s85
	s_addc_u32 s37, s31, 0
	s_add_i32 s55, s55, s68
	global_load_lds_dwordx4 v[178:179], off
	v_lshl_add_u64 v[178:179], s[36:37], 0, v[170:171]
	s_mov_b32 m0, s55
	s_add_i32 s65, s55, 0x2000
	global_load_lds_dwordx4 v[178:179], off
	v_lshl_add_u64 v[178:179], s[36:37], 0, v[172:173]
	s_mov_b32 m0, s65
	v_readlane_b32 s26, v253, 37
	global_load_lds_dwordx4 v[178:179], off
	s_mov_b32 m0, s69
	v_readlane_b32 s27, v253, 38
	s_nop 4
	global_load_lds_dwordx4 v34, s[26:27]
	s_mov_b32 m0, s70
	s_nop 0
	global_load_lds_dwordx4 v192, s[26:27]
	s_mov_b32 vcc_lo, s32
	s_mov_b32 vcc_hi, 0
	s_cbranch_vccz .Lw8_m0
	s_waitcnt vmcnt(12)
	s_branch .Lwd_m0

.Lwd_m0:
	s_waitcnt lgkmcnt(0)
	s_barrier
	s_setprio 1
	s_waitcnt lgkmcnt(0)
	v_mfma_f32_16x16x128_f8f6f4 v[96:99], v[26:33], v[202:209], 0
	v_mfma_f32_16x16x128_f8f6f4 v[92:95], v[18:25], v[202:209], 0
	v_mfma_f32_16x16x128_f8f6f4 v[84:87], v[18:25], v[222:229], 0
	v_mfma_f32_16x16x128_f8f6f4 v[88:91], v[26:33], v[222:229], 0
	v_mfma_f32_16x16x128_f8f6f4 v[80:83], v[26:33], v[230:237], 0
	v_mfma_f32_16x16x128_f8f6f4 v[76:79], v[18:25], v[230:237], 0
	v_mfma_f32_16x16x128_f8f6f4 v[68:71], v[18:25], v[238:245], 0
	v_mfma_f32_16x16x128_f8f6f4 v[72:75], v[26:33], v[238:245], 0
	s_setprio 0
	s_setprio 1
	v_mfma_f32_16x16x128_f8f6f4 v[64:67], v[10:17], v[202:209], 0
	v_mfma_f32_16x16x128_f8f6f4 v[60:63], v[2:9], v[202:209], 0
	v_mfma_f32_16x16x128_f8f6f4 v[52:55], v[2:9], v[222:229], 0
	v_mfma_f32_16x16x128_f8f6f4 v[56:59], v[10:17], v[222:229], 0
	v_mfma_f32_16x16x128_f8f6f4 v[48:51], v[10:17], v[230:237], 0
	v_mfma_f32_16x16x128_f8f6f4 v[44:47], v[2:9], v[230:237], 0
	v_mfma_f32_16x16x128_f8f6f4 v[36:39], v[2:9], v[238:245], 0
	v_mfma_f32_16x16x128_f8f6f4 v[40:43], v[10:17], v[238:245], 0
	s_setprio 0
	s_barrier
	s_add_i32 s54, 0, 0x18000
	s_add_i32 s51, 0, 0x1c000
	v_add_u32_e32 v201, s54, v167
	v_add_u32_e32 v202, s51, v167
	ds_read_b128 v[26:29], v201
	ds_read_b128 v[30:33], v201 offset:1024
	ds_read_b128 v[18:21], v201 offset:2048
	ds_read_b128 v[22:25], v201 offset:3072
	ds_read_b128 v[10:13], v202
	ds_read_b128 v[14:17], v202 offset:1024
	ds_read_b128 v[2:5], v202 offset:2048
	ds_read_b128 v[6:9], v202 offset:3072
	s_mov_b32 m0, s71
	ds_read_b128 v[204:207], v169 offset:32768
	ds_read_b128 v[208:211], v169 offset:33792
	ds_read_b128 v[222:225], v169 offset:34816
	ds_read_b128 v[226:229], v169 offset:35840
	ds_read_b128 v[230:233], v169 offset:36864
	ds_read_b128 v[234:237], v169 offset:37888
	ds_read_b128 v[238:241], v169 offset:38912
	ds_read_b128 v[242:245], v169 offset:39936
	global_load_lds_dwordx4 v189, s[26:27]
	s_mov_b32 m0, s72
	s_nop 0
	global_load_lds_dwordx4 v198, s[26:27]
	s_waitcnt vmcnt(8)
	s_waitcnt lgkmcnt(0)
	s_barrier
	s_setprio 1
	s_waitcnt lgkmcnt(0)
	v_mfma_f32_16x16x128_f8f6f4 v[160:163], v[26:33], v[204:211], v[160:163]
	v_mfma_f32_16x16x128_f8f6f4 v[156:159], v[18:25], v[204:211], v[156:159]
	v_mfma_f32_16x16x128_f8f6f4 v[148:151], v[18:25], v[222:229], v[148:151]
	v_mfma_f32_16x16x128_f8f6f4 v[152:155], v[26:33], v[222:229], v[152:155]
	v_mfma_f32_16x16x128_f8f6f4 v[144:147], v[26:33], v[230:237], v[144:147]
	v_mfma_f32_16x16x128_f8f6f4 v[140:143], v[18:25], v[230:237], v[140:143]
	v_mfma_f32_16x16x128_f8f6f4 v[132:135], v[18:25], v[238:245], v[132:135]
	v_mfma_f32_16x16x128_f8f6f4 v[136:139], v[26:33], v[238:245], v[136:139]
	s_setprio 0
	s_setprio 1
	v_mfma_f32_16x16x128_f8f6f4 v[128:131], v[10:17], v[204:211], v[128:131]
	v_mfma_f32_16x16x128_f8f6f4 v[124:127], v[2:9], v[204:211], v[124:127]
	v_mfma_f32_16x16x128_f8f6f4 v[116:119], v[2:9], v[222:229], v[116:119]
	v_mfma_f32_16x16x128_f8f6f4 v[120:123], v[10:17], v[222:229], v[120:123]
	v_mfma_f32_16x16x128_f8f6f4 v[112:115], v[10:17], v[230:237], v[112:115]
	v_mfma_f32_16x16x128_f8f6f4 v[108:111], v[2:9], v[230:237], v[108:111]
	v_mfma_f32_16x16x128_f8f6f4 v[100:103], v[2:9], v[238:245], v[100:103]
	v_mfma_f32_16x16x128_f8f6f4 v[104:107], v[10:17], v[238:245], v[104:107]
	s_setprio 0
	s_barrier
	s_add_i32 s54, s54, s68
	s_mov_b64 s[26:27], 0x180
	s_add_i32 s50, s54, 0x2000
	v_lshl_add_u64 v[178:179], v[194:195], 0, s[26:27]
	s_mov_b32 m0, s54
	s_add_u32 s30, s30, 0x20180
	ds_read_b128 v[204:207], v169 offset:49152
	ds_read_b128 v[208:211], v169 offset:50176
	ds_read_b128 v[222:225], v169 offset:51200
	ds_read_b128 v[226:229], v169 offset:52224
	ds_read_b128 v[230:233], v169 offset:53248
	ds_read_b128 v[234:237], v169 offset:54272
	ds_read_b128 v[238:241], v169 offset:55296
	ds_read_b128 v[242:245], v169 offset:56320
	global_load_lds_dwordx4 v[178:179], off
	v_lshl_add_u64 v[178:179], v[196:197], 0, s[26:27]
	s_mov_b32 m0, s50
	s_addc_u32 s31, s31, 0
	s_add_i32 s51, s51, s68
	global_load_lds_dwordx4 v[178:179], off
	v_lshl_add_u64 v[178:179], s[30:31], 0, v[170:171]
	s_mov_b32 m0, s51
	s_add_i32 s64, s51, 0x2000
	global_load_lds_dwordx4 v[178:179], off
	v_lshl_add_u64 v[178:179], s[30:31], 0, v[172:173]
	s_mov_b32 m0, s64
	v_readlane_b32 s26, v253, 39
	global_load_lds_dwordx4 v[178:179], off
	s_mov_b32 m0, s75
	v_readlane_b32 s27, v253, 40
	s_nop 4
	global_load_lds_dwordx4 v34, s[26:27]
	s_mov_b32 m0, s76
	s_nop 0
	global_load_lds_dwordx4 v192, s[26:27]
	s_waitcnt vmcnt(8)
	s_waitcnt lgkmcnt(0)
	s_barrier
	s_setprio 1
	s_waitcnt lgkmcnt(0)
	v_mfma_f32_16x16x128_f8f6f4 v[96:99], v[26:33], v[204:211], v[96:99]
	v_mfma_f32_16x16x128_f8f6f4 v[92:95], v[18:25], v[204:211], v[92:95]
	v_mfma_f32_16x16x128_f8f6f4 v[84:87], v[18:25], v[222:229], v[84:87]
	v_mfma_f32_16x16x128_f8f6f4 v[88:91], v[26:33], v[222:229], v[88:91]
	v_mfma_f32_16x16x128_f8f6f4 v[80:83], v[26:33], v[230:237], v[80:83]
	v_mfma_f32_16x16x128_f8f6f4 v[76:79], v[18:25], v[230:237], v[76:79]
	v_mfma_f32_16x16x128_f8f6f4 v[68:71], v[18:25], v[238:245], v[68:71]
	v_mfma_f32_16x16x128_f8f6f4 v[72:75], v[26:33], v[238:245], v[72:75]
	s_setprio 0
	s_setprio 1
	v_mfma_f32_16x16x128_f8f6f4 v[64:67], v[10:17], v[204:211], v[64:67]
	v_mfma_f32_16x16x128_f8f6f4 v[60:63], v[2:9], v[204:211], v[60:63]
	v_mfma_f32_16x16x128_f8f6f4 v[52:55], v[2:9], v[222:229], v[52:55]
	v_mfma_f32_16x16x128_f8f6f4 v[56:59], v[10:17], v[222:229], v[56:59]
	v_mfma_f32_16x16x128_f8f6f4 v[48:51], v[10:17], v[230:237], v[48:51]
	v_mfma_f32_16x16x128_f8f6f4 v[44:47], v[2:9], v[230:237], v[44:47]
	v_mfma_f32_16x16x128_f8f6f4 v[36:39], v[2:9], v[238:245], v[36:39]
	v_mfma_f32_16x16x128_f8f6f4 v[40:43], v[10:17], v[238:245], v[40:43]
	s_setprio 0
	s_barrier
	v_lshl_add_u64 v[18:19], s[26:27], 0, v[174:175]
	v_lshl_add_u64 v[20:21], s[26:27], 0, v[190:191]
	s_mov_b32 s63, 0
	s_mov_b64 s[30:31], 0
	s_branch .LBB0_821

.Lepi_nobar_0:
	v_pk_mul_f32 v[10:11], v[146:147], v[114:115]
	v_exp_f32_e64 v14, -v144
	v_exp_f32_e64 v15, -v145
	v_pk_mul_f32 v[10:11], v[18:19], v[10:11]
	v_exp_f32_e64 v18, -v142
	v_exp_f32_e64 v19, -v143
	v_pk_add_f32 v[14:15], v[14:15], 1.0 op_sel_hi:[1,0]
	v_pk_mul_f32 v[12:13], v[144:145], v[112:113]
	v_rcp_f32_e32 v14, v14
	v_rcp_f32_e32 v15, v15
	v_pk_add_f32 v[18:19], v[18:19], 1.0 op_sel_hi:[1,0]
	v_add_u32_e32 v7, 32, v6
	v_rcp_f32_e32 v18, v18
	v_rcp_f32_e32 v19, v19
	v_pk_mul_f32 v[12:13], v[14:15], v[12:13]
	v_pk_mul_f32 v[14:15], v[142:143], v[110:111]
	v_mad_i64_i32 v[8:9], s[30:31], v7, s14, v[4:5]
	v_pk_mul_f32 v[14:15], v[18:19], v[14:15]
	v_exp_f32_e64 v18, -v132
	v_exp_f32_e64 v19, -v133
	v_med3_f32 v7, v12, s13, v250
	v_med3_f32 v12, v13, s13, v250
	v_med3_f32 v13, v10, s13, v250
	v_mov_b32_e32 v10, v35
	v_cvt_pk_fp8_f32 v10, v7, v12
	v_pk_add_f32 v[18:19], v[18:19], 1.0 op_sel_hi:[1,0]
	v_med3_f32 v11, v11, s13, v250
	v_rcp_f32_e32 v18, v18
	v_rcp_f32_e32 v19, v19
	v_cvt_pk_fp8_f32 v10, v13, v11 op_sel:[0,0,1]
	v_med3_f32 v7, v16, s13, v250
	v_med3_f32 v12, v17, s13, v250
	v_mov_b32_e32 v11, v35
	v_pk_mul_f32 v[16:17], v[132:133], v[100:101]
	v_cvt_pk_fp8_f32 v11, v7, v12
	v_pk_mul_f32 v[16:17], v[18:19], v[16:17]
	v_exp_f32_e64 v18, -v138
	v_exp_f32_e64 v19, -v139
	v_med3_f32 v13, v14, s13, v250
	v_med3_f32 v14, v15, s13, v250
	v_cvt_pk_fp8_f32 v11, v13, v14 op_sel:[0,0,1]
	v_pk_add_f32 v[18:19], v[18:19], 1.0 op_sel_hi:[1,0]
	v_lshl_add_u64 v[8:9], v[8:9], 0, v[2:3]
	v_rcp_f32_e32 v18, v18
	v_rcp_f32_e32 v19, v19
	global_store_dwordx2 v[8:9], v[10:11], off
	v_pk_mul_f32 v[10:11], v[138:139], v[106:107]
	v_exp_f32_e64 v14, -v136
	v_exp_f32_e64 v15, -v137
	v_pk_mul_f32 v[10:11], v[18:19], v[10:11]
	v_exp_f32_e64 v18, -v134
	v_exp_f32_e64 v19, -v135
	v_pk_add_f32 v[14:15], v[14:15], 1.0 op_sel_hi:[1,0]
	v_pk_mul_f32 v[12:13], v[136:137], v[104:105]
	v_rcp_f32_e32 v14, v14
	v_rcp_f32_e32 v15, v15
	v_pk_add_f32 v[18:19], v[18:19], 1.0 op_sel_hi:[1,0]
	v_add_u32_e32 v7, 48, v6
	v_rcp_f32_e32 v18, v18
	v_rcp_f32_e32 v19, v19
	v_pk_mul_f32 v[12:13], v[14:15], v[12:13]
	v_pk_mul_f32 v[14:15], v[134:135], v[102:103]
	v_mad_i64_i32 v[8:9], s[30:31], v7, s14, v[4:5]
	v_pk_mul_f32 v[14:15], v[18:19], v[14:15]
	v_exp_f32_e64 v18, -v92
	v_exp_f32_e64 v19, -v93
	v_med3_f32 v7, v12, s13, v250
	v_med3_f32 v12, v13, s13, v250
	v_med3_f32 v13, v10, s13, v250
	v_mov_b32_e32 v10, v35
	v_cvt_pk_fp8_f32 v10, v7, v12
	v_pk_add_f32 v[18:19], v[18:19], 1.0 op_sel_hi:[1,0]
	v_med3_f32 v11, v11, s13, v250
	v_rcp_f32_e32 v18, v18
	v_rcp_f32_e32 v19, v19
	v_cvt_pk_fp8_f32 v10, v13, v11 op_sel:[0,0,1]
	v_med3_f32 v7, v16, s13, v250
	v_med3_f32 v12, v17, s13, v250
	v_mov_b32_e32 v11, v35
	v_pk_mul_f32 v[16:17], v[92:93], v[60:61]
	v_cvt_pk_fp8_f32 v11, v7, v12
	v_pk_mul_f32 v[16:17], v[18:19], v[16:17]
	v_exp_f32_e64 v18, -v98
	v_exp_f32_e64 v19, -v99
	v_med3_f32 v13, v14, s13, v250
	v_med3_f32 v14, v15, s13, v250
	v_cvt_pk_fp8_f32 v11, v13, v14 op_sel:[0,0,1]
	v_pk_add_f32 v[18:19], v[18:19], 1.0 op_sel_hi:[1,0]
	v_lshl_add_u64 v[8:9], v[8:9], 0, v[2:3]
	v_rcp_f32_e32 v18, v18
	v_rcp_f32_e32 v19, v19
	global_store_dwordx2 v[8:9], v[10:11], off
	v_add_u32_e32 v7, 0x80, v6
	v_mad_i64_i32 v[182:183], s[30:31], v7, s14, v[4:5]
	v_lshl_add_u64 v[182:183], v[182:183], 0, v[2:3]
	s_mov_b32 s32, 1
	s_and_b64 vcc, exec, s[6:7]
	s_mov_b64 s[84:85], s[24:25]
	s_cbranch_vccnz .LBB0_828
	s_andn2_b64 vcc, exec, s[10:11]
	s_cbranch_vccnz .LBB0_810
	s_barrier
	s_branch .LBB0_810

.LBB0_829:
	v_exp_f32_e64 v212, -v96
	v_exp_f32_e64 v213, -v97
	v_exp_f32_e64 v214, -v98
	v_exp_f32_e64 v215, -v99
	v_pk_mul_f32 v[216:217], v[96:97], v[64:65]
	v_pk_mul_f32 v[218:219], v[98:99], v[66:67]
	v_pk_add_f32 v[212:213], v[212:213], 1.0 op_sel_hi:[1,0]
	v_pk_add_f32 v[214:215], v[214:215], 1.0 op_sel_hi:[1,0]
	v_rcp_f32_e32 v212, v212
	v_rcp_f32_e32 v213, v213
	v_rcp_f32_e32 v214, v214
	v_rcp_f32_e32 v215, v215
	v_mov_b32_e32 v180, v35
	v_pk_mul_f32 v[216:217], v[212:213], v[216:217]
	v_pk_mul_f32 v[218:219], v[214:215], v[218:219]
	v_med3_f32 v216, v216, s13, v250
	v_med3_f32 v217, v217, s13, v250
	v_med3_f32 v218, v218, s13, v250
	v_med3_f32 v219, v219, s13, v250
	v_cvt_pk_fp8_f32 v180, v216, v217
	s_nop 0
	v_cvt_pk_fp8_f32 v180, v218, v219 op_sel:[0,0,1]
	v_exp_f32_e64 v212, -v92
	v_exp_f32_e64 v213, -v93
	v_exp_f32_e64 v214, -v94
	v_exp_f32_e64 v215, -v95
	v_pk_mul_f32 v[216:217], v[92:93], v[60:61]
	v_pk_mul_f32 v[218:219], v[94:95], v[62:63]
	v_pk_add_f32 v[212:213], v[212:213], 1.0 op_sel_hi:[1,0]
	v_pk_add_f32 v[214:215], v[214:215], 1.0 op_sel_hi:[1,0]
	v_rcp_f32_e32 v212, v212
	v_rcp_f32_e32 v213, v213
	v_rcp_f32_e32 v214, v214
	v_rcp_f32_e32 v215, v215
	v_mov_b32_e32 v181, v35
	v_pk_mul_f32 v[216:217], v[212:213], v[216:217]
	v_pk_mul_f32 v[218:219], v[214:215], v[218:219]
	v_med3_f32 v216, v216, s13, v250
	v_med3_f32 v217, v217, s13, v250
	v_med3_f32 v218, v218, s13, v250
	v_med3_f32 v219, v219, s13, v250
	v_cvt_pk_fp8_f32 v181, v216, v217
	s_nop 0
	v_cvt_pk_fp8_f32 v181, v218, v219 op_sel:[0,0,1]
	s_nop 0
	global_store_dwordx2 v[182:183], v[180:181], off
	v_add_co_u32_e32 v182, vcc, 0xe000, v182
	s_nop 1
	v_addc_co_u32_e32 v183, vcc, 0, v183, vcc
	v_exp_f32_e64 v212, -v88
	v_exp_f32_e64 v213, -v89
	v_exp_f32_e64 v214, -v90
	v_exp_f32_e64 v215, -v91
	v_pk_mul_f32 v[216:217], v[88:89], v[56:57]
	v_pk_mul_f32 v[218:219], v[90:91], v[58:59]
	v_pk_add_f32 v[212:213], v[212:213], 1.0 op_sel_hi:[1,0]
	v_pk_add_f32 v[214:215], v[214:215], 1.0 op_sel_hi:[1,0]
	v_rcp_f32_e32 v212, v212
	v_rcp_f32_e32 v213, v213
	v_rcp_f32_e32 v214, v214
	v_rcp_f32_e32 v215, v215
	v_mov_b32_e32 v180, v35
	v_pk_mul_f32 v[216:217], v[212:213], v[216:217]
	v_pk_mul_f32 v[218:219], v[214:215], v[218:219]
	v_med3_f32 v216, v216, s13, v250
	v_med3_f32 v217, v217, s13, v250
	v_med3_f32 v218, v218, s13, v250
	v_med3_f32 v219, v219, s13, v250
	v_cvt_pk_fp8_f32 v180, v216, v217
	s_nop 0
	v_cvt_pk_fp8_f32 v180, v218, v219 op_sel:[0,0,1]
	v_exp_f32_e64 v212, -v84
	v_exp_f32_e64 v213, -v85
	v_exp_f32_e64 v214, -v86
	v_exp_f32_e64 v215, -v87
	v_pk_mul_f32 v[216:217], v[84:85], v[52:53]
	v_pk_mul_f32 v[218:219], v[86:87], v[54:55]
	v_pk_add_f32 v[212:213], v[212:213], 1.0 op_sel_hi:[1,0]
	v_pk_add_f32 v[214:215], v[214:215], 1.0 op_sel_hi:[1,0]
	v_rcp_f32_e32 v212, v212
	v_rcp_f32_e32 v213, v213
	v_rcp_f32_e32 v214, v214
	v_rcp_f32_e32 v215, v215
	v_mov_b32_e32 v181, v35
	v_pk_mul_f32 v[216:217], v[212:213], v[216:217]
	v_pk_mul_f32 v[218:219], v[214:215], v[218:219]
	v_med3_f32 v216, v216, s13, v250
	v_med3_f32 v217, v217, s13, v250
	v_med3_f32 v218, v218, s13, v250
	v_med3_f32 v219, v219, s13, v250
	v_cvt_pk_fp8_f32 v181, v216, v217
	s_nop 0
	v_cvt_pk_fp8_f32 v181, v218, v219 op_sel:[0,0,1]
	s_nop 0
	global_store_dwordx2 v[182:183], v[180:181], off
	v_add_co_u32_e32 v182, vcc, 0xe000, v182
	s_nop 1
	v_addc_co_u32_e32 v183, vcc, 0, v183, vcc
	v_exp_f32_e64 v212, -v80
	v_exp_f32_e64 v213, -v81
	v_exp_f32_e64 v214, -v82
	v_exp_f32_e64 v215, -v83
	v_pk_mul_f32 v[216:217], v[80:81], v[48:49]
	v_pk_mul_f32 v[218:219], v[82:83], v[50:51]
	v_pk_add_f32 v[212:213], v[212:213], 1.0 op_sel_hi:[1,0]
	v_pk_add_f32 v[214:215], v[214:215], 1.0 op_sel_hi:[1,0]
	v_rcp_f32_e32 v212, v212
	v_rcp_f32_e32 v213, v213
	v_rcp_f32_e32 v214, v214
	v_rcp_f32_e32 v215, v215
	v_mov_b32_e32 v180, v35
	v_pk_mul_f32 v[216:217], v[212:213], v[216:217]
	v_pk_mul_f32 v[218:219], v[214:215], v[218:219]
	v_med3_f32 v216, v216, s13, v250
	v_med3_f32 v217, v217, s13, v250
	v_med3_f32 v218, v218, s13, v250
	v_med3_f32 v219, v219, s13, v250
	v_cvt_pk_fp8_f32 v180, v216, v217
	s_nop 0
	v_cvt_pk_fp8_f32 v180, v218, v219 op_sel:[0,0,1]
	v_exp_f32_e64 v212, -v76
	v_exp_f32_e64 v213, -v77
	v_exp_f32_e64 v214, -v78
	v_exp_f32_e64 v215, -v79
	v_pk_mul_f32 v[216:217], v[76:77], v[44:45]
	v_pk_mul_f32 v[218:219], v[78:79], v[46:47]
	v_pk_add_f32 v[212:213], v[212:213], 1.0 op_sel_hi:[1,0]
	v_pk_add_f32 v[214:215], v[214:215], 1.0 op_sel_hi:[1,0]
	v_rcp_f32_e32 v212, v212
	v_rcp_f32_e32 v213, v213
	v_rcp_f32_e32 v214, v214
	v_rcp_f32_e32 v215, v215
	v_mov_b32_e32 v181, v35
	v_pk_mul_f32 v[216:217], v[212:213], v[216:217]
	v_pk_mul_f32 v[218:219], v[214:215], v[218:219]
	v_med3_f32 v216, v216, s13, v250
	v_med3_f32 v217, v217, s13, v250
	v_med3_f32 v218, v218, s13, v250
	v_med3_f32 v219, v219, s13, v250
	v_cvt_pk_fp8_f32 v181, v216, v217
	s_nop 0
	v_cvt_pk_fp8_f32 v181, v218, v219 op_sel:[0,0,1]
	s_nop 0
	global_store_dwordx2 v[182:183], v[180:181], off
	v_add_co_u32_e32 v182, vcc, 0xe000, v182
	s_nop 1
	v_addc_co_u32_e32 v183, vcc, 0, v183, vcc
	v_exp_f32_e64 v212, -v72
	v_exp_f32_e64 v213, -v73
	v_exp_f32_e64 v214, -v74
	v_exp_f32_e64 v215, -v75
	v_pk_mul_f32 v[216:217], v[72:73], v[40:41]
	v_pk_mul_f32 v[218:219], v[74:75], v[42:43]
	v_pk_add_f32 v[212:213], v[212:213], 1.0 op_sel_hi:[1,0]
	v_pk_add_f32 v[214:215], v[214:215], 1.0 op_sel_hi:[1,0]
	v_rcp_f32_e32 v212, v212
	v_rcp_f32_e32 v213, v213
	v_rcp_f32_e32 v214, v214
	v_rcp_f32_e32 v215, v215
	v_mov_b32_e32 v180, v35
	v_pk_mul_f32 v[216:217], v[212:213], v[216:217]
	v_pk_mul_f32 v[218:219], v[214:215], v[218:219]
	v_med3_f32 v216, v216, s13, v250
	v_med3_f32 v217, v217, s13, v250
	v_med3_f32 v218, v218, s13, v250
	v_med3_f32 v219, v219, s13, v250
	v_cvt_pk_fp8_f32 v180, v216, v217
	s_nop 0
	v_cvt_pk_fp8_f32 v180, v218, v219 op_sel:[0,0,1]
	v_exp_f32_e64 v212, -v68
	v_exp_f32_e64 v213, -v69
	v_exp_f32_e64 v214, -v70
	v_exp_f32_e64 v215, -v71
	v_pk_mul_f32 v[216:217], v[68:69], v[36:37]
	v_pk_mul_f32 v[218:219], v[70:71], v[38:39]
	v_pk_add_f32 v[212:213], v[212:213], 1.0 op_sel_hi:[1,0]
	v_pk_add_f32 v[214:215], v[214:215], 1.0 op_sel_hi:[1,0]
	v_rcp_f32_e32 v212, v212
	v_rcp_f32_e32 v213, v213
	v_rcp_f32_e32 v214, v214
	v_rcp_f32_e32 v215, v215
	v_mov_b32_e32 v181, v35
	v_pk_mul_f32 v[216:217], v[212:213], v[216:217]
	v_pk_mul_f32 v[218:219], v[214:215], v[218:219]
	v_med3_f32 v216, v216, s13, v250
	v_med3_f32 v217, v217, s13, v250
	v_med3_f32 v218, v218, s13, v250
	v_med3_f32 v219, v219, s13, v250
	v_cvt_pk_fp8_f32 v181, v216, v217
	s_nop 0
	v_cvt_pk_fp8_f32 v181, v218, v219 op_sel:[0,0,1]
	s_nop 0
	global_store_dwordx2 v[182:183], v[180:181], off
	s_waitcnt vmcnt(0)
	v_readlane_b32 s80, v254, 51
	v_readlane_b32 s78, v254, 59
	v_readlane_b32 s74, v255, 3
	v_readlane_b32 s76, v255, 5
	v_readlane_b32 s81, v254, 52
	v_readlane_b32 s82, v254, 53
	v_readlane_b32 s83, v254, 54
	v_readlane_b32 s79, v254, 60
	v_readlane_b32 s75, v255, 4
	v_readlane_b32 s77, v255, 6
	v_readlane_b32 s67, v255, 28
	v_readlane_b32 s71, v255, 26
	v_readlane_b32 s26, v255, 23
	s_barrier

.LBB0_934:
	s_bitcmp1_b32 s47, 0
	s_cselect_b32 s14, 0x7700000, 0
	v_readlane_b32 s22, v253, 26
	v_bfe_u32 v165, v168, 4, 2
	v_readlane_b32 s23, v253, 27
	s_add_u32 s22, s22, s14
	v_and_b32_e32 v1, 15, v168
	v_lshlrev_b32_e32 v6, 4, v165
	v_lshlrev_b32_e32 v7, 2, v168
	s_addc_u32 s23, s23, 0
	v_lshl_or_b32 v6, v1, 6, v6
	s_lshl_b32 s14, s36, 13
	v_and_b32_e32 v7, 32, v7
	v_bitop3_b32 v8, v6, s14, v7 bitop3:0xde
	s_lshl_b32 s14, s37, 5
	s_and_b32 s89, s14, 0x60
	s_add_i32 m0, s52, 0x18000
	v_lshl_add_u64 v[4:5], v[4:5], 0, s[18:19]
	v_readlane_b32 s26, v253, 28
	s_lshl_b32 s87, s36, 6
	s_lshl_b32 s14, s89, 7
	s_waitcnt vmcnt(2)
	s_barrier
	global_load_lds_dwordx4 v[4:5], off
	v_lshl_add_u64 v[2:3], v[2:3], 0, s[18:19]
	s_add_i32 m0, s52, 0x1a000
	v_readlane_b32 s27, v253, 29
	s_add_i32 s90, s52, 0x8000
	s_add_i32 s91, s52, 0xa000
	v_mov_b32_e32 v193, v35
	global_load_lds_dwordx4 v[2:3], off
	v_lshl_add_u64 v[2:3], s[26:27], 0, v[34:35]
	s_mov_b32 m0, s90
	s_add_u32 s36, s30, 0x20080
	global_load_lds_dwordx4 v[2:3], off
	v_lshl_add_u64 v[2:3], s[26:27], 0, v[192:193]
	s_mov_b32 m0, s91
	s_addc_u32 s37, s31, 0
	global_load_lds_dwordx4 v[2:3], off
	s_add_i32 m0, s52, 0x1c000
	v_lshl_add_u64 v[2:3], s[36:37], 0, v[170:171]
	global_load_lds_dwordx4 v[2:3], off
	v_lshl_add_u64 v[2:3], s[36:37], 0, v[172:173]
	s_add_i32 m0, s52, 0x1e000
	v_mov_b32_e32 v36, 0
	global_load_lds_dwordx4 v[2:3], off
	s_waitcnt vmcnt(6)
	s_cmpk_lt_u32 s46, 0x100
	s_mov_b32 s88, 0
	v_bitop3_b32 v167, v6, s14, v7 bitop3:0xde
	s_cselect_b64 s[36:37], -1, 0
	v_add_u32_e32 v169, 0, v8
	v_mov_b32_e32 v198, v174
	v_mov_b32_e32 v189, v190
	v_mov_b32_e32 v37, v36
	v_mov_b32_e32 v38, v36
	v_mov_b32_e32 v39, v36
	v_mov_b32_e32 v40, v36
	v_mov_b32_e32 v41, v36
	v_mov_b32_e32 v42, v36
	v_mov_b32_e32 v43, v36
	v_mov_b32_e32 v44, v36
	v_mov_b32_e32 v45, v36
	v_mov_b32_e32 v46, v36
	v_mov_b32_e32 v47, v36
	v_mov_b32_e32 v48, v36
	v_mov_b32_e32 v49, v36
	v_mov_b32_e32 v50, v36
	v_mov_b32_e32 v51, v36
	v_mov_b32_e32 v52, v36
	v_mov_b32_e32 v53, v36
	v_mov_b32_e32 v54, v36
	v_mov_b32_e32 v55, v36
	v_mov_b32_e32 v56, v36
	v_mov_b32_e32 v57, v36
	v_mov_b32_e32 v58, v36
	v_mov_b32_e32 v59, v36
	v_mov_b32_e32 v60, v36
	v_mov_b32_e32 v61, v36
	v_mov_b32_e32 v62, v36
	v_mov_b32_e32 v63, v36
	v_mov_b32_e32 v64, v36
	v_mov_b32_e32 v65, v36
	v_mov_b32_e32 v66, v36
	v_mov_b32_e32 v67, v36
	v_mov_b32_e32 v68, v36
	v_mov_b32_e32 v69, v36
	v_mov_b32_e32 v70, v36
	v_mov_b32_e32 v71, v36
	v_mov_b32_e32 v72, v36
	v_mov_b32_e32 v73, v36
	v_mov_b32_e32 v74, v36
	v_mov_b32_e32 v75, v36
	v_mov_b32_e32 v76, v36
	v_mov_b32_e32 v77, v36
	v_mov_b32_e32 v78, v36
	v_mov_b32_e32 v79, v36
	v_mov_b32_e32 v80, v36
	v_mov_b32_e32 v81, v36
	v_mov_b32_e32 v82, v36
	v_mov_b32_e32 v83, v36
	v_mov_b32_e32 v84, v36
	v_mov_b32_e32 v85, v36
	v_mov_b32_e32 v86, v36
	v_mov_b32_e32 v87, v36
	v_mov_b32_e32 v88, v36
	v_mov_b32_e32 v89, v36
	v_mov_b32_e32 v90, v36
	v_mov_b32_e32 v91, v36
	v_mov_b32_e32 v92, v36
	v_mov_b32_e32 v93, v36
	v_mov_b32_e32 v94, v36
	v_mov_b32_e32 v95, v36
	v_mov_b32_e32 v96, v36
	v_mov_b32_e32 v97, v36
	v_mov_b32_e32 v98, v36
	v_mov_b32_e32 v99, v36
	v_mov_b32_e32 v100, v36
	v_mov_b32_e32 v101, v36
	v_mov_b32_e32 v102, v36
	v_mov_b32_e32 v103, v36
	v_mov_b32_e32 v104, v36
	v_mov_b32_e32 v105, v36
	v_mov_b32_e32 v106, v36
	v_mov_b32_e32 v107, v36
	v_mov_b32_e32 v108, v36
	v_mov_b32_e32 v109, v36
	v_mov_b32_e32 v110, v36
	v_mov_b32_e32 v111, v36
	v_mov_b32_e32 v112, v36
	v_mov_b32_e32 v113, v36
	v_mov_b32_e32 v114, v36
	v_mov_b32_e32 v115, v36
	v_mov_b32_e32 v116, v36
	v_mov_b32_e32 v117, v36
	v_mov_b32_e32 v118, v36
	v_mov_b32_e32 v119, v36
	v_mov_b32_e32 v120, v36
	v_mov_b32_e32 v121, v36
	v_mov_b32_e32 v122, v36
	v_mov_b32_e32 v123, v36
	v_mov_b32_e32 v124, v36
	v_mov_b32_e32 v125, v36
	v_mov_b32_e32 v126, v36
	v_mov_b32_e32 v127, v36
	v_mov_b32_e32 v128, v36
	v_mov_b32_e32 v129, v36
	v_mov_b32_e32 v130, v36
	v_mov_b32_e32 v131, v36
	v_mov_b32_e32 v132, v36
	v_mov_b32_e32 v133, v36
	v_mov_b32_e32 v134, v36
	v_mov_b32_e32 v135, v36
	v_mov_b32_e32 v136, v36
	v_mov_b32_e32 v137, v36
	v_mov_b32_e32 v138, v36
	v_mov_b32_e32 v139, v36
	v_mov_b32_e32 v140, v36
	v_mov_b32_e32 v141, v36
	v_mov_b32_e32 v142, v36
	v_mov_b32_e32 v143, v36
	v_mov_b32_e32 v144, v36
	v_mov_b32_e32 v145, v36
	v_mov_b32_e32 v146, v36
	v_mov_b32_e32 v147, v36
	v_mov_b32_e32 v148, v36
	v_mov_b32_e32 v149, v36
	v_mov_b32_e32 v150, v36
	v_mov_b32_e32 v151, v36
	v_mov_b32_e32 v152, v36
	v_mov_b32_e32 v153, v36
	v_mov_b32_e32 v154, v36
	v_mov_b32_e32 v155, v36
	v_mov_b32_e32 v156, v36
	v_mov_b32_e32 v157, v36
	v_mov_b32_e32 v158, v36
	v_mov_b32_e32 v159, v36
	v_mov_b32_e32 v160, v36
	v_mov_b32_e32 v161, v36
	v_mov_b32_e32 v162, v36
	v_mov_b32_e32 v163, v36
	s_barrier
	s_mov_b32 s32, 0
	s_branch .LBB0_936

.LBB0_953:
	s_add_u32 s95, s30, 0x200
	s_addc_u32 s96, s31, 0
	s_add_i32 s65, 0, 0x14000
	s_add_i32 s67, 0, 0x10000
	v_add_u32_e32 v199, s65, v167
	v_add_u32_e32 v200, s67, v167
	ds_read_b128 v[10:13], v199
	ds_read_b128 v[14:17], v199 offset:1024
	ds_read_b128 v[2:5], v199 offset:2048
	ds_read_b128 v[6:9], v199 offset:3072
	ds_read_b128 v[22:25], v200 offset:3072
	ds_read_b128 v[18:21], v200 offset:2048
	ds_read_b128 v[30:33], v200 offset:1024
	ds_read_b128 v[26:29], v200
	s_lshl_b32 s14, s94, 10
	s_add_i32 s97, s14, 0
	s_add_i32 s97, s97, 0x20400
	v_mov_b32_e32 v191, v35
	v_mov_b32_e32 v175, v35
	s_add_i32 s83, s52, 0xc000
	v_readlane_b32 s26, v253, 28
	s_mov_b32 m0, s83
	v_readlane_b32 s27, v253, 29
	s_add_i32 s53, s52, 0xe000
	ds_read_b128 v[178:181], v169
	ds_read_b128 v[182:185], v169 offset:1024
	ds_read_b128 v[202:205], v169 offset:2048
	ds_read_b128 v[206:209], v169 offset:3072
	ds_read_b128 v[210:213], v169 offset:4096
	ds_read_b128 v[214:217], v169 offset:5120
	ds_read_b128 v[222:225], v169 offset:6144
	ds_read_b128 v[226:229], v169 offset:7168
	global_load_lds_dwordx4 v190, s[26:27]
	s_mov_b32 m0, s53
	s_nop 0
	global_load_lds_dwordx4 v174, s[26:27]
	s_waitcnt vmcnt(8)
	s_waitcnt lgkmcnt(0)
	s_barrier
	s_setprio 1
	s_waitcnt lgkmcnt(0)
	s_mov_b32 vcc_lo, s32
	s_mov_b32 vcc_hi, 0
	s_cbranch_vccz .Lc1p_m1
	v_mfma_f32_16x16x128_f8f6f4 v[160:163], v[26:33], v[178:185], 0
	v_exp_f32_e64 v234, -v96
	v_exp_f32_e64 v235, -v97
	v_exp_f32_e64 v236, -v98
	v_exp_f32_e64 v237, -v99
	v_pk_mul_f32 v[238:239], v[96:97], v[64:65]
	v_mfma_f32_16x16x128_f8f6f4 v[156:159], v[18:25], v[178:185], 0
	v_pk_mul_f32 v[240:241], v[98:99], v[66:67]
	v_pk_add_f32 v[234:235], v[234:235], 1.0 op_sel_hi:[1,0]
	v_pk_add_f32 v[236:237], v[236:237], 1.0 op_sel_hi:[1,0]
	v_rcp_f32_e32 v234, v234
	v_rcp_f32_e32 v235, v235
	v_mfma_f32_16x16x128_f8f6f4 v[148:151], v[18:25], v[202:209], 0
	v_rcp_f32_e32 v236, v236
	v_rcp_f32_e32 v237, v237
	v_mov_b32_e32 v232, v35
	v_pk_mul_f32 v[238:239], v[234:235], v[238:239]
	v_pk_mul_f32 v[240:241], v[236:237], v[240:241]
	v_mfma_f32_16x16x128_f8f6f4 v[152:155], v[26:33], v[202:209], 0
	v_med3_f32 v238, v238, s13, v250
	v_med3_f32 v239, v239, s13, v250
	v_med3_f32 v240, v240, s13, v250
	v_med3_f32 v241, v241, s13, v250
	v_cvt_pk_fp8_f32 v232, v238, v239
	v_mfma_f32_16x16x128_f8f6f4 v[144:147], v[26:33], v[210:217], 0
	s_nop 0
	v_cvt_pk_fp8_f32 v232, v240, v241 op_sel:[0,0,1]
	v_exp_f32_e64 v234, -v92
	v_exp_f32_e64 v235, -v93
	v_exp_f32_e64 v236, -v94
	v_mfma_f32_16x16x128_f8f6f4 v[140:143], v[18:25], v[210:217], 0
	v_exp_f32_e64 v237, -v95
	v_pk_mul_f32 v[238:239], v[92:93], v[60:61]
	v_pk_mul_f32 v[240:241], v[94:95], v[62:63]
	v_pk_add_f32 v[234:235], v[234:235], 1.0 op_sel_hi:[1,0]
	v_pk_add_f32 v[236:237], v[236:237], 1.0 op_sel_hi:[1,0]
	v_mfma_f32_16x16x128_f8f6f4 v[132:135], v[18:25], v[222:229], 0
	v_rcp_f32_e32 v234, v234
	v_rcp_f32_e32 v235, v235
	v_rcp_f32_e32 v236, v236
	v_rcp_f32_e32 v237, v237
	v_mov_b32_e32 v233, v35
	v_mfma_f32_16x16x128_f8f6f4 v[136:139], v[26:33], v[222:229], 0
	v_pk_mul_f32 v[238:239], v[234:235], v[238:239]
	v_pk_mul_f32 v[240:241], v[236:237], v[240:241]
	v_med3_f32 v238, v238, s13, v250
	v_med3_f32 v239, v239, s13, v250
	v_med3_f32 v240, v240, s13, v250
	s_setprio 0
	s_setprio 1
	v_mfma_f32_16x16x128_f8f6f4 v[128:131], v[10:17], v[178:185], 0
	v_med3_f32 v241, v241, s13, v250
	v_cvt_pk_fp8_f32 v233, v238, v239
	s_nop 0
	v_cvt_pk_fp8_f32 v233, v240, v241 op_sel:[0,0,1]
	s_nop 0
	v_mfma_f32_16x16x128_f8f6f4 v[124:127], v[2:9], v[178:185], 0
	global_store_dwordx2 v[230:231], v[232:233], off
	v_add_co_u32_e32 v230, vcc, 0xe000, v230
	s_nop 1
	v_addc_co_u32_e32 v231, vcc, 0, v231, vcc
	v_exp_f32_e64 v234, -v88
	v_mfma_f32_16x16x128_f8f6f4 v[116:119], v[2:9], v[202:209], 0
	v_exp_f32_e64 v235, -v89
	v_exp_f32_e64 v236, -v90
	v_exp_f32_e64 v237, -v91
	v_pk_mul_f32 v[238:239], v[88:89], v[56:57]
	v_pk_mul_f32 v[240:241], v[90:91], v[58:59]
	v_mfma_f32_16x16x128_f8f6f4 v[120:123], v[10:17], v[202:209], 0
	v_pk_add_f32 v[234:235], v[234:235], 1.0 op_sel_hi:[1,0]
	v_pk_add_f32 v[236:237], v[236:237], 1.0 op_sel_hi:[1,0]
	v_rcp_f32_e32 v234, v234
	v_rcp_f32_e32 v235, v235
	v_rcp_f32_e32 v236, v236
	v_mfma_f32_16x16x128_f8f6f4 v[112:115], v[10:17], v[210:217], 0
	v_rcp_f32_e32 v237, v237
	v_mov_b32_e32 v232, v35
	v_pk_mul_f32 v[238:239], v[234:235], v[238:239]
	v_pk_mul_f32 v[240:241], v[236:237], v[240:241]
	v_med3_f32 v238, v238, s13, v250
	v_mfma_f32_16x16x128_f8f6f4 v[108:111], v[2:9], v[210:217], 0
	v_med3_f32 v239, v239, s13, v250
	v_med3_f32 v240, v240, s13, v250
	v_med3_f32 v241, v241, s13, v250
	v_cvt_pk_fp8_f32 v232, v238, v239
	s_nop 0
	v_mfma_f32_16x16x128_f8f6f4 v[100:103], v[2:9], v[222:229], 0
	v_cvt_pk_fp8_f32 v232, v240, v241 op_sel:[0,0,1]
	v_mfma_f32_16x16x128_f8f6f4 v[104:107], v[10:17], v[222:229], 0
	s_branch .Lc1d_m1
.Lc1p_m1:
	v_mfma_f32_16x16x128_f8f6f4 v[160:163], v[26:33], v[178:185], 0
	v_mfma_f32_16x16x128_f8f6f4 v[156:159], v[18:25], v[178:185], 0
	v_mfma_f32_16x16x128_f8f6f4 v[148:151], v[18:25], v[202:209], 0
	v_mfma_f32_16x16x128_f8f6f4 v[152:155], v[26:33], v[202:209], 0
	v_mfma_f32_16x16x128_f8f6f4 v[144:147], v[26:33], v[210:217], 0
	v_mfma_f32_16x16x128_f8f6f4 v[140:143], v[18:25], v[210:217], 0
	v_mfma_f32_16x16x128_f8f6f4 v[132:135], v[18:25], v[222:229], 0
	v_mfma_f32_16x16x128_f8f6f4 v[136:139], v[26:33], v[222:229], 0
	s_setprio 0
	s_setprio 1
	v_mfma_f32_16x16x128_f8f6f4 v[128:131], v[10:17], v[178:185], 0
	v_mfma_f32_16x16x128_f8f6f4 v[124:127], v[2:9], v[178:185], 0
	v_mfma_f32_16x16x128_f8f6f4 v[116:119], v[2:9], v[202:209], 0
	v_mfma_f32_16x16x128_f8f6f4 v[120:123], v[10:17], v[202:209], 0
	v_mfma_f32_16x16x128_f8f6f4 v[112:115], v[10:17], v[210:217], 0
	v_mfma_f32_16x16x128_f8f6f4 v[108:111], v[2:9], v[210:217], 0
	v_mfma_f32_16x16x128_f8f6f4 v[100:103], v[2:9], v[222:229], 0
	v_mfma_f32_16x16x128_f8f6f4 v[104:107], v[10:17], v[222:229], 0
.Lc1d_m1:
	s_setprio 0
	s_barrier
	v_lshl_add_u64 v[194:195], s[30:31], 0, v[170:171]
	s_add_i32 s67, s67, s82
	v_lshl_add_u64 v[196:197], v[194:195], 0, s[28:29]
	s_mov_b32 m0, s67
	s_add_i32 s55, s67, 0x2000
	ds_read_b128 v[178:181], v169 offset:16384
	ds_read_b128 v[182:185], v169 offset:17408
	ds_read_b128 v[202:205], v169 offset:18432
	ds_read_b128 v[206:209], v169 offset:19456
	ds_read_b128 v[210:213], v169 offset:20480
	ds_read_b128 v[214:217], v169 offset:21504
	ds_read_b128 v[222:225], v169 offset:22528
	ds_read_b128 v[226:229], v169 offset:23552
	s_mov_b32 vcc_lo, s32
	s_mov_b32 vcc_hi, 0
	s_cbranch_vccz .Le1skip_m1
	v_exp_f32_e64 v234, -v84
	v_exp_f32_e64 v235, -v85
	v_exp_f32_e64 v236, -v86
	v_exp_f32_e64 v237, -v87
	v_pk_mul_f32 v[238:239], v[84:85], v[52:53]
	v_pk_mul_f32 v[240:241], v[86:87], v[54:55]
	v_pk_add_f32 v[234:235], v[234:235], 1.0 op_sel_hi:[1,0]
	v_pk_add_f32 v[236:237], v[236:237], 1.0 op_sel_hi:[1,0]
	v_rcp_f32_e32 v234, v234
	v_rcp_f32_e32 v235, v235
	v_rcp_f32_e32 v236, v236
	v_rcp_f32_e32 v237, v237
	v_mov_b32_e32 v233, v35
	v_pk_mul_f32 v[238:239], v[234:235], v[238:239]
	v_pk_mul_f32 v[240:241], v[236:237], v[240:241]
	v_med3_f32 v238, v238, s13, v250
	v_med3_f32 v239, v239, s13, v250
	v_med3_f32 v240, v240, s13, v250
	v_med3_f32 v241, v241, s13, v250
	v_cvt_pk_fp8_f32 v233, v238, v239
	s_nop 0
	v_cvt_pk_fp8_f32 v233, v240, v241 op_sel:[0,0,1]
	s_nop 0
	global_store_dwordx2 v[230:231], v[232:233], off
	v_add_co_u32_e32 v230, vcc, 0xe000, v230
	s_nop 1
	v_addc_co_u32_e32 v231, vcc, 0, v231, vcc
	v_exp_f32_e64 v234, -v80
	v_exp_f32_e64 v235, -v81
	v_exp_f32_e64 v236, -v82
	v_exp_f32_e64 v237, -v83
	v_pk_mul_f32 v[238:239], v[80:81], v[48:49]
	v_pk_mul_f32 v[240:241], v[82:83], v[50:51]
	v_pk_add_f32 v[234:235], v[234:235], 1.0 op_sel_hi:[1,0]
	v_pk_add_f32 v[236:237], v[236:237], 1.0 op_sel_hi:[1,0]
	v_rcp_f32_e32 v234, v234
	v_rcp_f32_e32 v235, v235
	v_rcp_f32_e32 v236, v236
	v_rcp_f32_e32 v237, v237
	v_mov_b32_e32 v232, v35
	v_pk_mul_f32 v[238:239], v[234:235], v[238:239]
	v_pk_mul_f32 v[240:241], v[236:237], v[240:241]
	v_med3_f32 v238, v238, s13, v250
	v_med3_f32 v239, v239, s13, v250
	v_med3_f32 v240, v240, s13, v250
	v_med3_f32 v241, v241, s13, v250
	v_cvt_pk_fp8_f32 v232, v238, v239
	s_nop 0
	v_cvt_pk_fp8_f32 v232, v240, v241 op_sel:[0,0,1]
	v_exp_f32_e64 v234, -v76
	v_exp_f32_e64 v235, -v77
	v_exp_f32_e64 v236, -v78
	v_exp_f32_e64 v237, -v79
	v_pk_mul_f32 v[238:239], v[76:77], v[44:45]
	v_pk_mul_f32 v[240:241], v[78:79], v[46:47]
	v_pk_add_f32 v[234:235], v[234:235], 1.0 op_sel_hi:[1,0]
	v_pk_add_f32 v[236:237], v[236:237], 1.0 op_sel_hi:[1,0]
	v_rcp_f32_e32 v234, v234
	v_rcp_f32_e32 v235, v235
	v_rcp_f32_e32 v236, v236
	v_rcp_f32_e32 v237, v237
	v_mov_b32_e32 v233, v35
	v_pk_mul_f32 v[238:239], v[234:235], v[238:239]
	v_pk_mul_f32 v[240:241], v[236:237], v[240:241]
	v_med3_f32 v238, v238, s13, v250
	v_med3_f32 v239, v239, s13, v250
	v_med3_f32 v240, v240, s13, v250
	v_med3_f32 v241, v241, s13, v250
	v_cvt_pk_fp8_f32 v233, v238, v239
	s_nop 0
	v_cvt_pk_fp8_f32 v233, v240, v241 op_sel:[0,0,1]
	s_nop 0
	global_store_dwordx2 v[230:231], v[232:233], off
	v_add_co_u32_e32 v230, vcc, 0xe000, v230
	s_nop 1
	v_addc_co_u32_e32 v231, vcc, 0, v231, vcc
	v_exp_f32_e64 v234, -v72
	v_exp_f32_e64 v235, -v73
	v_exp_f32_e64 v236, -v74
	v_exp_f32_e64 v237, -v75
	v_pk_mul_f32 v[238:239], v[72:73], v[40:41]
	v_pk_mul_f32 v[240:241], v[74:75], v[42:43]
	v_pk_add_f32 v[234:235], v[234:235], 1.0 op_sel_hi:[1,0]
	v_pk_add_f32 v[236:237], v[236:237], 1.0 op_sel_hi:[1,0]
	v_rcp_f32_e32 v234, v234
	v_rcp_f32_e32 v235, v235
	v_rcp_f32_e32 v236, v236
	v_rcp_f32_e32 v237, v237
	v_mov_b32_e32 v232, v35
	v_pk_mul_f32 v[238:239], v[234:235], v[238:239]
	v_pk_mul_f32 v[240:241], v[236:237], v[240:241]
	v_med3_f32 v238, v238, s13, v250
	v_med3_f32 v239, v239, s13, v250
	v_med3_f32 v240, v240, s13, v250
	v_med3_f32 v241, v241, s13, v250
	v_cvt_pk_fp8_f32 v232, v238, v239
	s_nop 0
	v_cvt_pk_fp8_f32 v232, v240, v241 op_sel:[0,0,1]
	v_exp_f32_e64 v234, -v68
	v_exp_f32_e64 v235, -v69
	v_exp_f32_e64 v236, -v70
	v_exp_f32_e64 v237, -v71
	v_pk_mul_f32 v[238:239], v[68:69], v[36:37]
	v_pk_mul_f32 v[240:241], v[70:71], v[38:39]
	v_pk_add_f32 v[234:235], v[234:235], 1.0 op_sel_hi:[1,0]
	v_pk_add_f32 v[236:237], v[236:237], 1.0 op_sel_hi:[1,0]
	v_rcp_f32_e32 v234, v234
	v_rcp_f32_e32 v235, v235
	v_rcp_f32_e32 v236, v236
	v_rcp_f32_e32 v237, v237
	v_mov_b32_e32 v233, v35
	v_pk_mul_f32 v[238:239], v[234:235], v[238:239]
	v_pk_mul_f32 v[240:241], v[236:237], v[240:241]
	v_med3_f32 v238, v238, s13, v250
	v_med3_f32 v239, v239, s13, v250
	v_med3_f32 v240, v240, s13, v250
	v_med3_f32 v241, v241, s13, v250
	v_cvt_pk_fp8_f32 v233, v238, v239
	s_nop 0
	v_cvt_pk_fp8_f32 v233, v240, v241 op_sel:[0,0,1]
	s_nop 0
	global_store_dwordx2 v[230:231], v[232:233], off
.Le1skip_m1:
	global_load_lds_dwordx4 v[196:197], off
	v_lshl_add_u64 v[196:197], s[30:31], 0, v[172:173]
	s_add_u32 s46, s30, 0x20100
	v_lshl_add_u64 v[218:219], v[196:197], 0, s[28:29]
	s_mov_b32 m0, s55
	s_addc_u32 s47, s31, 0
	s_add_i32 s65, s65, s82
	global_load_lds_dwordx4 v[218:219], off
	v_lshl_add_u64 v[218:219], s[46:47], 0, v[170:171]
	s_mov_b32 m0, s65
	s_add_i32 s54, s65, 0x2000
	global_load_lds_dwordx4 v[218:219], off
	v_lshl_add_u64 v[218:219], s[46:47], 0, v[172:173]
	s_mov_b32 m0, s54
	v_readlane_b32 s26, v253, 37
	global_load_lds_dwordx4 v[218:219], off
	s_mov_b32 m0, s52
	v_readlane_b32 s27, v253, 38
	s_nop 4
	global_load_lds_dwordx4 v34, s[26:27]
	s_mov_b32 m0, s84
	s_nop 0
	global_load_lds_dwordx4 v192, s[26:27]
	s_mov_b32 vcc_lo, s32
	s_mov_b32 vcc_hi, 0
	s_cbranch_vccz .Lw8_m1
	s_waitcnt vmcnt(12)
	s_branch .Lwd_m1

.Lwd_m1:
	s_waitcnt lgkmcnt(0)
	s_barrier
	s_setprio 1
	s_waitcnt lgkmcnt(0)
	v_mfma_f32_16x16x128_f8f6f4 v[96:99], v[26:33], v[178:185], 0
	v_mfma_f32_16x16x128_f8f6f4 v[92:95], v[18:25], v[178:185], 0
	v_mfma_f32_16x16x128_f8f6f4 v[84:87], v[18:25], v[202:209], 0
	v_mfma_f32_16x16x128_f8f6f4 v[88:91], v[26:33], v[202:209], 0
	v_mfma_f32_16x16x128_f8f6f4 v[80:83], v[26:33], v[210:217], 0
	v_mfma_f32_16x16x128_f8f6f4 v[76:79], v[18:25], v[210:217], 0
	v_mfma_f32_16x16x128_f8f6f4 v[68:71], v[18:25], v[222:229], 0
	v_mfma_f32_16x16x128_f8f6f4 v[72:75], v[26:33], v[222:229], 0
	s_setprio 0
	s_setprio 1
	v_mfma_f32_16x16x128_f8f6f4 v[64:67], v[10:17], v[178:185], 0
	v_mfma_f32_16x16x128_f8f6f4 v[60:63], v[2:9], v[178:185], 0
	v_mfma_f32_16x16x128_f8f6f4 v[52:55], v[2:9], v[202:209], 0
	v_mfma_f32_16x16x128_f8f6f4 v[56:59], v[10:17], v[202:209], 0
	v_mfma_f32_16x16x128_f8f6f4 v[48:51], v[10:17], v[210:217], 0
	v_mfma_f32_16x16x128_f8f6f4 v[44:47], v[2:9], v[210:217], 0
	v_mfma_f32_16x16x128_f8f6f4 v[36:39], v[2:9], v[222:229], 0
	v_mfma_f32_16x16x128_f8f6f4 v[40:43], v[10:17], v[222:229], 0
	s_setprio 0
	s_barrier
	s_add_i32 s50, 0, 0x18000
	s_add_i32 s64, 0, 0x1c000
	v_add_u32_e32 v201, s50, v167
	v_add_u32_e32 v202, s64, v167
	ds_read_b128 v[26:29], v201
	ds_read_b128 v[30:33], v201 offset:1024
	ds_read_b128 v[18:21], v201 offset:2048
	ds_read_b128 v[22:25], v201 offset:3072
	ds_read_b128 v[10:13], v202
	ds_read_b128 v[14:17], v202 offset:1024
	ds_read_b128 v[2:5], v202 offset:2048
	ds_read_b128 v[6:9], v202 offset:3072
	s_mov_b32 m0, s85
	ds_read_b128 v[178:181], v169 offset:32768
	ds_read_b128 v[182:185], v169 offset:33792
	ds_read_b128 v[204:207], v169 offset:34816
	ds_read_b128 v[208:211], v169 offset:35840
	ds_read_b128 v[212:215], v169 offset:36864
	ds_read_b128 v[216:219], v169 offset:37888
	ds_read_b128 v[222:225], v169 offset:38912
	ds_read_b128 v[226:229], v169 offset:39936
	global_load_lds_dwordx4 v189, s[26:27]
	s_mov_b32 m0, s86
	s_nop 0
	global_load_lds_dwordx4 v198, s[26:27]
	s_waitcnt vmcnt(8)
	s_waitcnt lgkmcnt(0)
	s_barrier
	s_setprio 1
	s_waitcnt lgkmcnt(0)
	v_mfma_f32_16x16x128_f8f6f4 v[160:163], v[26:33], v[178:185], v[160:163]
	v_mfma_f32_16x16x128_f8f6f4 v[156:159], v[18:25], v[178:185], v[156:159]
	v_mfma_f32_16x16x128_f8f6f4 v[148:151], v[18:25], v[204:211], v[148:151]
	v_mfma_f32_16x16x128_f8f6f4 v[152:155], v[26:33], v[204:211], v[152:155]
	v_mfma_f32_16x16x128_f8f6f4 v[144:147], v[26:33], v[212:219], v[144:147]
	v_mfma_f32_16x16x128_f8f6f4 v[140:143], v[18:25], v[212:219], v[140:143]
	v_mfma_f32_16x16x128_f8f6f4 v[132:135], v[18:25], v[222:229], v[132:135]
	v_mfma_f32_16x16x128_f8f6f4 v[136:139], v[26:33], v[222:229], v[136:139]
	s_setprio 0
	s_setprio 1
	v_mfma_f32_16x16x128_f8f6f4 v[128:131], v[10:17], v[178:185], v[128:131]
	v_mfma_f32_16x16x128_f8f6f4 v[124:127], v[2:9], v[178:185], v[124:127]
	v_mfma_f32_16x16x128_f8f6f4 v[116:119], v[2:9], v[204:211], v[116:119]
	v_mfma_f32_16x16x128_f8f6f4 v[120:123], v[10:17], v[204:211], v[120:123]
	v_mfma_f32_16x16x128_f8f6f4 v[112:115], v[10:17], v[212:219], v[112:115]
	v_mfma_f32_16x16x128_f8f6f4 v[108:111], v[2:9], v[212:219], v[108:111]
	v_mfma_f32_16x16x128_f8f6f4 v[100:103], v[2:9], v[222:229], v[100:103]
	v_mfma_f32_16x16x128_f8f6f4 v[104:107], v[10:17], v[222:229], v[104:107]
	s_setprio 0
	s_barrier
	s_add_i32 s50, s50, s82
	s_mov_b64 s[26:27], 0x180
	s_add_i32 s51, s50, 0x2000
	v_lshl_add_u64 v[194:195], v[194:195], 0, s[26:27]
	s_mov_b32 m0, s50
	s_add_u32 s30, s30, 0x20180
	ds_read_b128 v[178:181], v169 offset:49152
	ds_read_b128 v[182:185], v169 offset:50176
	ds_read_b128 v[204:207], v169 offset:51200
	ds_read_b128 v[208:211], v169 offset:52224
	ds_read_b128 v[212:215], v169 offset:53248
	ds_read_b128 v[216:219], v169 offset:54272
	ds_read_b128 v[222:225], v169 offset:55296
	ds_read_b128 v[226:229], v169 offset:56320
	global_load_lds_dwordx4 v[194:195], off
	v_lshl_add_u64 v[194:195], v[196:197], 0, s[26:27]
	s_mov_b32 m0, s51
	s_addc_u32 s31, s31, 0
	s_add_i32 s64, s64, s82
	global_load_lds_dwordx4 v[194:195], off
	v_lshl_add_u64 v[194:195], s[30:31], 0, v[170:171]
	s_mov_b32 m0, s64
	s_add_i32 s63, s64, 0x2000
	global_load_lds_dwordx4 v[194:195], off
	v_lshl_add_u64 v[194:195], s[30:31], 0, v[172:173]
	s_mov_b32 m0, s63
	v_readlane_b32 s26, v253, 39
	global_load_lds_dwordx4 v[194:195], off
	s_mov_b32 m0, s90
	v_readlane_b32 s27, v253, 40
	s_nop 4
	global_load_lds_dwordx4 v34, s[26:27]
	s_mov_b32 m0, s91
	s_nop 0
	global_load_lds_dwordx4 v192, s[26:27]
	s_waitcnt vmcnt(8)
	s_waitcnt lgkmcnt(0)
	s_barrier
	s_setprio 1
	s_waitcnt lgkmcnt(0)
	v_mfma_f32_16x16x128_f8f6f4 v[96:99], v[26:33], v[178:185], v[96:99]
	v_mfma_f32_16x16x128_f8f6f4 v[92:95], v[18:25], v[178:185], v[92:95]
	v_mfma_f32_16x16x128_f8f6f4 v[84:87], v[18:25], v[204:211], v[84:87]
	v_mfma_f32_16x16x128_f8f6f4 v[88:91], v[26:33], v[204:211], v[88:91]
	v_mfma_f32_16x16x128_f8f6f4 v[80:83], v[26:33], v[212:219], v[80:83]
	v_mfma_f32_16x16x128_f8f6f4 v[76:79], v[18:25], v[212:219], v[76:79]
	v_mfma_f32_16x16x128_f8f6f4 v[68:71], v[18:25], v[222:229], v[68:71]
	v_mfma_f32_16x16x128_f8f6f4 v[72:75], v[26:33], v[222:229], v[72:75]
	s_setprio 0
	s_setprio 1
	v_mfma_f32_16x16x128_f8f6f4 v[64:67], v[10:17], v[178:185], v[64:67]
	v_mfma_f32_16x16x128_f8f6f4 v[60:63], v[2:9], v[178:185], v[60:63]
	v_mfma_f32_16x16x128_f8f6f4 v[52:55], v[2:9], v[204:211], v[52:55]
	v_mfma_f32_16x16x128_f8f6f4 v[56:59], v[10:17], v[204:211], v[56:59]
	v_mfma_f32_16x16x128_f8f6f4 v[48:51], v[10:17], v[212:219], v[48:51]
	v_mfma_f32_16x16x128_f8f6f4 v[44:47], v[2:9], v[212:219], v[44:47]
	v_mfma_f32_16x16x128_f8f6f4 v[36:39], v[2:9], v[222:229], v[36:39]
	v_mfma_f32_16x16x128_f8f6f4 v[40:43], v[10:17], v[222:229], v[40:43]
	s_setprio 0
	s_barrier
	v_lshl_add_u64 v[18:19], s[26:27], 0, v[174:175]
	v_lshl_add_u64 v[20:21], s[26:27], 0, v[190:191]
	s_mov_b32 s75, 0
	s_mov_b64 s[30:31], 0
	s_branch .LBB0_955

.Lepi_nobar_1:
	v_pk_mul_f32 v[10:11], v[146:147], v[114:115]
	v_exp_f32_e64 v14, -v144
	v_exp_f32_e64 v15, -v145
	v_pk_mul_f32 v[10:11], v[18:19], v[10:11]
	v_exp_f32_e64 v18, -v142
	v_exp_f32_e64 v19, -v143
	v_pk_add_f32 v[14:15], v[14:15], 1.0 op_sel_hi:[1,0]
	v_pk_mul_f32 v[12:13], v[144:145], v[112:113]
	v_rcp_f32_e32 v14, v14
	v_rcp_f32_e32 v15, v15
	v_pk_add_f32 v[18:19], v[18:19], 1.0 op_sel_hi:[1,0]
	v_add_u32_e32 v7, 32, v6
	v_rcp_f32_e32 v18, v18
	v_rcp_f32_e32 v19, v19
	v_pk_mul_f32 v[12:13], v[14:15], v[12:13]
	v_pk_mul_f32 v[14:15], v[142:143], v[110:111]
	v_mad_i64_i32 v[8:9], s[46:47], v7, s14, v[4:5]
	v_pk_mul_f32 v[14:15], v[18:19], v[14:15]
	v_exp_f32_e64 v18, -v132
	v_exp_f32_e64 v19, -v133
	v_med3_f32 v7, v12, s13, v250
	v_med3_f32 v12, v13, s13, v250
	v_med3_f32 v13, v10, s13, v250
	v_mov_b32_e32 v10, v35
	v_cvt_pk_fp8_f32 v10, v7, v12
	v_pk_add_f32 v[18:19], v[18:19], 1.0 op_sel_hi:[1,0]
	v_med3_f32 v11, v11, s13, v250
	v_rcp_f32_e32 v18, v18
	v_rcp_f32_e32 v19, v19
	v_cvt_pk_fp8_f32 v10, v13, v11 op_sel:[0,0,1]
	v_med3_f32 v7, v16, s13, v250
	v_med3_f32 v12, v17, s13, v250
	v_mov_b32_e32 v11, v35
	v_pk_mul_f32 v[16:17], v[132:133], v[100:101]
	v_cvt_pk_fp8_f32 v11, v7, v12
	v_pk_mul_f32 v[16:17], v[18:19], v[16:17]
	v_exp_f32_e64 v18, -v138
	v_exp_f32_e64 v19, -v139
	v_med3_f32 v13, v14, s13, v250
	v_med3_f32 v14, v15, s13, v250
	v_cvt_pk_fp8_f32 v11, v13, v14 op_sel:[0,0,1]
	v_pk_add_f32 v[18:19], v[18:19], 1.0 op_sel_hi:[1,0]
	v_lshl_add_u64 v[8:9], v[8:9], 0, v[2:3]
	v_rcp_f32_e32 v18, v18
	v_rcp_f32_e32 v19, v19
	global_store_dwordx2 v[8:9], v[10:11], off
	v_pk_mul_f32 v[10:11], v[138:139], v[106:107]
	v_exp_f32_e64 v14, -v136
	v_exp_f32_e64 v15, -v137
	v_pk_mul_f32 v[10:11], v[18:19], v[10:11]
	v_exp_f32_e64 v18, -v134
	v_exp_f32_e64 v19, -v135
	v_pk_add_f32 v[14:15], v[14:15], 1.0 op_sel_hi:[1,0]
	v_pk_mul_f32 v[12:13], v[136:137], v[104:105]
	v_rcp_f32_e32 v14, v14
	v_rcp_f32_e32 v15, v15
	v_pk_add_f32 v[18:19], v[18:19], 1.0 op_sel_hi:[1,0]
	v_add_u32_e32 v7, 48, v6
	v_rcp_f32_e32 v18, v18
	v_rcp_f32_e32 v19, v19
	v_pk_mul_f32 v[12:13], v[14:15], v[12:13]
	v_pk_mul_f32 v[14:15], v[134:135], v[102:103]
	v_mad_i64_i32 v[8:9], s[46:47], v7, s14, v[4:5]
	v_pk_mul_f32 v[14:15], v[18:19], v[14:15]
	v_exp_f32_e64 v18, -v92
	v_exp_f32_e64 v19, -v93
	v_med3_f32 v7, v12, s13, v250
	v_med3_f32 v12, v13, s13, v250
	v_med3_f32 v13, v10, s13, v250
	v_mov_b32_e32 v10, v35
	v_cvt_pk_fp8_f32 v10, v7, v12
	v_pk_add_f32 v[18:19], v[18:19], 1.0 op_sel_hi:[1,0]
	v_med3_f32 v11, v11, s13, v250
	v_rcp_f32_e32 v18, v18
	v_rcp_f32_e32 v19, v19
	v_cvt_pk_fp8_f32 v10, v13, v11 op_sel:[0,0,1]
	v_med3_f32 v7, v16, s13, v250
	v_med3_f32 v12, v17, s13, v250
	v_mov_b32_e32 v11, v35
	v_pk_mul_f32 v[16:17], v[92:93], v[60:61]
	v_cvt_pk_fp8_f32 v11, v7, v12
	v_pk_mul_f32 v[16:17], v[18:19], v[16:17]
	v_exp_f32_e64 v18, -v98
	v_exp_f32_e64 v19, -v99
	v_med3_f32 v13, v14, s13, v250
	v_med3_f32 v14, v15, s13, v250
	v_cvt_pk_fp8_f32 v11, v13, v14 op_sel:[0,0,1]
	v_pk_add_f32 v[18:19], v[18:19], 1.0 op_sel_hi:[1,0]
	v_lshl_add_u64 v[8:9], v[8:9], 0, v[2:3]
	v_rcp_f32_e32 v18, v18
	v_rcp_f32_e32 v19, v19
	global_store_dwordx2 v[8:9], v[10:11], off
	v_add_u32_e32 v7, 0x80, v6
	v_mad_i64_i32 v[230:231], s[46:47], v7, s14, v[4:5]
	v_lshl_add_u64 v[230:231], v[230:231], 0, v[2:3]
	s_mov_b32 s32, 1
	s_andn2_b64 vcc, exec, s[44:45]
	s_cbranch_vccnz .LBB0_962
	v_readlane_b32 s96, v254, 55
	s_andn2_b64 vcc, exec, s[6:7]
	v_readlane_b32 s95, v254, 48
	v_readlane_b32 s97, v254, 56
	s_cbranch_vccnz .LBB0_935
	s_barrier
	s_branch .LBB0_935

.LBB0_963:
	v_exp_f32_e64 v234, -v96
	v_exp_f32_e64 v235, -v97
	v_exp_f32_e64 v236, -v98
	v_exp_f32_e64 v237, -v99
	v_pk_mul_f32 v[238:239], v[96:97], v[64:65]
	v_pk_mul_f32 v[240:241], v[98:99], v[66:67]
	v_pk_add_f32 v[234:235], v[234:235], 1.0 op_sel_hi:[1,0]
	v_pk_add_f32 v[236:237], v[236:237], 1.0 op_sel_hi:[1,0]
	v_rcp_f32_e32 v234, v234
	v_rcp_f32_e32 v235, v235
	v_rcp_f32_e32 v236, v236
	v_rcp_f32_e32 v237, v237
	v_mov_b32_e32 v232, v35
	v_pk_mul_f32 v[238:239], v[234:235], v[238:239]
	v_pk_mul_f32 v[240:241], v[236:237], v[240:241]
	v_med3_f32 v238, v238, s13, v250
	v_med3_f32 v239, v239, s13, v250
	v_med3_f32 v240, v240, s13, v250
	v_med3_f32 v241, v241, s13, v250
	v_cvt_pk_fp8_f32 v232, v238, v239
	s_nop 0
	v_cvt_pk_fp8_f32 v232, v240, v241 op_sel:[0,0,1]
	v_exp_f32_e64 v234, -v92
	v_exp_f32_e64 v235, -v93
	v_exp_f32_e64 v236, -v94
	v_exp_f32_e64 v237, -v95
	v_pk_mul_f32 v[238:239], v[92:93], v[60:61]
	v_pk_mul_f32 v[240:241], v[94:95], v[62:63]
	v_pk_add_f32 v[234:235], v[234:235], 1.0 op_sel_hi:[1,0]
	v_pk_add_f32 v[236:237], v[236:237], 1.0 op_sel_hi:[1,0]
	v_rcp_f32_e32 v234, v234
	v_rcp_f32_e32 v235, v235
	v_rcp_f32_e32 v236, v236
	v_rcp_f32_e32 v237, v237
	v_mov_b32_e32 v233, v35
	v_pk_mul_f32 v[238:239], v[234:235], v[238:239]
	v_pk_mul_f32 v[240:241], v[236:237], v[240:241]
	v_med3_f32 v238, v238, s13, v250
	v_med3_f32 v239, v239, s13, v250
	v_med3_f32 v240, v240, s13, v250
	v_med3_f32 v241, v241, s13, v250
	v_cvt_pk_fp8_f32 v233, v238, v239
	s_nop 0
	v_cvt_pk_fp8_f32 v233, v240, v241 op_sel:[0,0,1]
	s_nop 0
	global_store_dwordx2 v[230:231], v[232:233], off
	v_add_co_u32_e32 v230, vcc, 0xe000, v230
	s_nop 1
	v_addc_co_u32_e32 v231, vcc, 0, v231, vcc
	v_exp_f32_e64 v234, -v88
	v_exp_f32_e64 v235, -v89
	v_exp_f32_e64 v236, -v90
	v_exp_f32_e64 v237, -v91
	v_pk_mul_f32 v[238:239], v[88:89], v[56:57]
	v_pk_mul_f32 v[240:241], v[90:91], v[58:59]
	v_pk_add_f32 v[234:235], v[234:235], 1.0 op_sel_hi:[1,0]
	v_pk_add_f32 v[236:237], v[236:237], 1.0 op_sel_hi:[1,0]
	v_rcp_f32_e32 v234, v234
	v_rcp_f32_e32 v235, v235
	v_rcp_f32_e32 v236, v236
	v_rcp_f32_e32 v237, v237
	v_mov_b32_e32 v232, v35
	v_pk_mul_f32 v[238:239], v[234:235], v[238:239]
	v_pk_mul_f32 v[240:241], v[236:237], v[240:241]
	v_med3_f32 v238, v238, s13, v250
	v_med3_f32 v239, v239, s13, v250
	v_med3_f32 v240, v240, s13, v250
	v_med3_f32 v241, v241, s13, v250
	v_cvt_pk_fp8_f32 v232, v238, v239
	s_nop 0
	v_cvt_pk_fp8_f32 v232, v240, v241 op_sel:[0,0,1]
	v_exp_f32_e64 v234, -v84
	v_exp_f32_e64 v235, -v85
	v_exp_f32_e64 v236, -v86
	v_exp_f32_e64 v237, -v87
	v_pk_mul_f32 v[238:239], v[84:85], v[52:53]
	v_pk_mul_f32 v[240:241], v[86:87], v[54:55]
	v_pk_add_f32 v[234:235], v[234:235], 1.0 op_sel_hi:[1,0]
	v_pk_add_f32 v[236:237], v[236:237], 1.0 op_sel_hi:[1,0]
	v_rcp_f32_e32 v234, v234
	v_rcp_f32_e32 v235, v235
	v_rcp_f32_e32 v236, v236
	v_rcp_f32_e32 v237, v237
	v_mov_b32_e32 v233, v35
	v_pk_mul_f32 v[238:239], v[234:235], v[238:239]
	v_pk_mul_f32 v[240:241], v[236:237], v[240:241]
	v_med3_f32 v238, v238, s13, v250
	v_med3_f32 v239, v239, s13, v250
	v_med3_f32 v240, v240, s13, v250
	v_med3_f32 v241, v241, s13, v250
	v_cvt_pk_fp8_f32 v233, v238, v239
	s_nop 0
	v_cvt_pk_fp8_f32 v233, v240, v241 op_sel:[0,0,1]
	s_nop 0
	global_store_dwordx2 v[230:231], v[232:233], off
	v_add_co_u32_e32 v230, vcc, 0xe000, v230
	s_nop 1
	v_addc_co_u32_e32 v231, vcc, 0, v231, vcc
	v_exp_f32_e64 v234, -v80
	v_exp_f32_e64 v235, -v81
	v_exp_f32_e64 v236, -v82
	v_exp_f32_e64 v237, -v83
	v_pk_mul_f32 v[238:239], v[80:81], v[48:49]
	v_pk_mul_f32 v[240:241], v[82:83], v[50:51]
	v_pk_add_f32 v[234:235], v[234:235], 1.0 op_sel_hi:[1,0]
	v_pk_add_f32 v[236:237], v[236:237], 1.0 op_sel_hi:[1,0]
	v_rcp_f32_e32 v234, v234
	v_rcp_f32_e32 v235, v235
	v_rcp_f32_e32 v236, v236
	v_rcp_f32_e32 v237, v237
	v_mov_b32_e32 v232, v35
	v_pk_mul_f32 v[238:239], v[234:235], v[238:239]
	v_pk_mul_f32 v[240:241], v[236:237], v[240:241]
	v_med3_f32 v238, v238, s13, v250
	v_med3_f32 v239, v239, s13, v250
	v_med3_f32 v240, v240, s13, v250
	v_med3_f32 v241, v241, s13, v250
	v_cvt_pk_fp8_f32 v232, v238, v239
	s_nop 0
	v_cvt_pk_fp8_f32 v232, v240, v241 op_sel:[0,0,1]
	v_exp_f32_e64 v234, -v76
	v_exp_f32_e64 v235, -v77
	v_exp_f32_e64 v236, -v78
	v_exp_f32_e64 v237, -v79
	v_pk_mul_f32 v[238:239], v[76:77], v[44:45]
	v_pk_mul_f32 v[240:241], v[78:79], v[46:47]
	v_pk_add_f32 v[234:235], v[234:235], 1.0 op_sel_hi:[1,0]
	v_pk_add_f32 v[236:237], v[236:237], 1.0 op_sel_hi:[1,0]
	v_rcp_f32_e32 v234, v234
	v_rcp_f32_e32 v235, v235
	v_rcp_f32_e32 v236, v236
	v_rcp_f32_e32 v237, v237
	v_mov_b32_e32 v233, v35
	v_pk_mul_f32 v[238:239], v[234:235], v[238:239]
	v_pk_mul_f32 v[240:241], v[236:237], v[240:241]
	v_med3_f32 v238, v238, s13, v250
	v_med3_f32 v239, v239, s13, v250
	v_med3_f32 v240, v240, s13, v250
	v_med3_f32 v241, v241, s13, v250
	v_cvt_pk_fp8_f32 v233, v238, v239
	s_nop 0
	v_cvt_pk_fp8_f32 v233, v240, v241 op_sel:[0,0,1]
	s_nop 0
	global_store_dwordx2 v[230:231], v[232:233], off
	v_add_co_u32_e32 v230, vcc, 0xe000, v230
	s_nop 1
	v_addc_co_u32_e32 v231, vcc, 0, v231, vcc
	v_exp_f32_e64 v234, -v72
	v_exp_f32_e64 v235, -v73
	v_exp_f32_e64 v236, -v74
	v_exp_f32_e64 v237, -v75
	v_pk_mul_f32 v[238:239], v[72:73], v[40:41]
	v_pk_mul_f32 v[240:241], v[74:75], v[42:43]
	v_pk_add_f32 v[234:235], v[234:235], 1.0 op_sel_hi:[1,0]
	v_pk_add_f32 v[236:237], v[236:237], 1.0 op_sel_hi:[1,0]
	v_rcp_f32_e32 v234, v234
	v_rcp_f32_e32 v235, v235
	v_rcp_f32_e32 v236, v236
	v_rcp_f32_e32 v237, v237
	v_mov_b32_e32 v232, v35
	v_pk_mul_f32 v[238:239], v[234:235], v[238:239]
	v_pk_mul_f32 v[240:241], v[236:237], v[240:241]
	v_med3_f32 v238, v238, s13, v250
	v_med3_f32 v239, v239, s13, v250
	v_med3_f32 v240, v240, s13, v250
	v_med3_f32 v241, v241, s13, v250
	v_cvt_pk_fp8_f32 v232, v238, v239
	s_nop 0
	v_cvt_pk_fp8_f32 v232, v240, v241 op_sel:[0,0,1]
	v_exp_f32_e64 v234, -v68
	v_exp_f32_e64 v235, -v69
	v_exp_f32_e64 v236, -v70
	v_exp_f32_e64 v237, -v71
	v_pk_mul_f32 v[238:239], v[68:69], v[36:37]
	v_pk_mul_f32 v[240:241], v[70:71], v[38:39]
	v_pk_add_f32 v[234:235], v[234:235], 1.0 op_sel_hi:[1,0]
	v_pk_add_f32 v[236:237], v[236:237], 1.0 op_sel_hi:[1,0]
	v_rcp_f32_e32 v234, v234
	v_rcp_f32_e32 v235, v235
	v_rcp_f32_e32 v236, v236
	v_rcp_f32_e32 v237, v237
	v_mov_b32_e32 v233, v35
	v_pk_mul_f32 v[238:239], v[234:235], v[238:239]
	v_pk_mul_f32 v[240:241], v[236:237], v[240:241]
	v_med3_f32 v238, v238, s13, v250
	v_med3_f32 v239, v239, s13, v250
	v_med3_f32 v240, v240, s13, v250
	v_med3_f32 v241, v241, s13, v250
	v_cvt_pk_fp8_f32 v233, v238, v239
	s_nop 0
	v_cvt_pk_fp8_f32 v233, v240, v241 op_sel:[0,0,1]
	s_nop 0
	global_store_dwordx2 v[230:231], v[232:233], off
	s_waitcnt vmcnt(0)
	v_readlane_b32 s90, v254, 49
	v_readlane_b32 s80, v254, 51
	v_readlane_b32 s78, v254, 59
	v_readlane_b32 s88, v254, 47
	v_readlane_b32 s91, v254, 50
	v_readlane_b32 s81, v254, 52
	v_readlane_b32 s82, v254, 53
	v_readlane_b32 s83, v254, 54
	s_mov_b64 s[92:93], s[0:1]
	v_readlane_b32 s79, v254, 60
	v_readlane_b32 s89, v255, 8
	v_readlane_b32 s94, v255, 9
	s_mov_b32 s85, s25
	v_readlane_b32 s87, v255, 24
	s_barrier
